# branch GEMM: gate loads of the mid-K hook and of the epilogue issued as one batch each (fresh registers, copies at the old sites), on top of the combine-phase gain hoist
# speedup vs baseline: 1.0010x; 1.0010x over previous
.LBB0_891:
	s_cmp_lg_u32 s0, 8
	s_cbranch_scc1 .LBB0_890
	s_nop 15
	s_nop 15
	v_mbcnt_lo_u32_b32 v3, -1, 0
	v_mbcnt_hi_u32_b32 v3, -1, v3
	s_nop 0
	v_and_b32_e32 v2, 15, v3
	v_ashrrev_i32_e32 v3, 1, v3
	v_add_u32_e32 v2, s85, v2
	v_and_b32_e32 v3, -8, v3
	v_add_u32_e32 v4, s86, v3
	v_ashrrev_i32_e32 v3, 31, v2
	v_lshlrev_b64 v[2:3], 11, v[2:3]
	v_lshl_add_u64 v[2:3], s[92:93], 0, v[2:3]
	v_ashrrev_i32_e32 v5, 31, v4
	v_lshl_add_u64 v[2:3], v[2:3], 0, v[4:5]
	global_load_dwordx2 v[188:189], v[2:3], off nt
	global_load_dwordx2 v[190:191], v[2:3], off offset:1024
	global_load_dwordx2 v[180:181], v[2:3], off offset:128 nt
	global_load_dwordx2 v[178:179], v[2:3], off offset:1152
	v_add_co_u32_e32 v6, vcc, s74, v2
	s_nop 1
	v_addc_co_u32_e32 v7, vcc, 0, v3, vcc
	global_load_dwordx2 v[206:207], v[6:7], off nt
	global_load_dwordx2 v[208:209], v[6:7], off offset:1024
	global_load_dwordx2 v[210:211], v[6:7], off offset:128 nt
	global_load_dwordx2 v[212:213], v[6:7], off offset:1152
	v_add_co_u32_e32 v6, vcc, s61, v2
	s_nop 1
	v_addc_co_u32_e32 v7, vcc, 0, v3, vcc
	global_load_dwordx2 v[214:215], v[6:7], off nt
	global_load_dwordx2 v[216:217], v[6:7], off offset:1024
	global_load_dwordx2 v[218:219], v[6:7], off offset:128 nt
	global_load_dwordx2 v[220:221], v[6:7], off offset:1152
	v_add_co_u32_e32 v6, vcc, s73, v2
	s_nop 1
	v_addc_co_u32_e32 v7, vcc, 0, v3, vcc
	global_load_dwordx2 v[222:223], v[6:7], off nt
	global_load_dwordx2 v[224:225], v[6:7], off offset:1024
	global_load_dwordx2 v[226:227], v[6:7], off offset:128 nt
	global_load_dwordx2 v[228:229], v[6:7], off offset:1152
	v_add_co_u32_e32 v6, vcc, s76, v2
	s_nop 1
	v_addc_co_u32_e32 v7, vcc, 0, v3, vcc
	global_load_dwordx2 v[230:231], v[6:7], off nt
	global_load_dwordx2 v[232:233], v[6:7], off offset:1024
	global_load_dwordx2 v[234:235], v[6:7], off offset:128 nt
	global_load_dwordx2 v[236:237], v[6:7], off offset:1152
	v_add_co_u32_e32 v6, vcc, s77, v2
	s_nop 1
	v_addc_co_u32_e32 v7, vcc, 0, v3, vcc
	global_load_dwordx2 v[238:239], v[6:7], off nt
	global_load_dwordx2 v[240:241], v[6:7], off offset:1024
	global_load_dwordx2 v[242:243], v[6:7], off offset:128 nt
	global_load_dwordx2 v[244:245], v[6:7], off offset:1152
	v_add_co_u32_e32 v6, vcc, s78, v2
	s_nop 1
	v_addc_co_u32_e32 v7, vcc, 0, v3, vcc
	global_load_dwordx2 v[246:247], v[6:7], off nt
	global_load_dwordx2 v[248:249], v[6:7], off offset:1024
	global_load_dwordx2 v[250:251], v[6:7], off offset:128 nt
	global_load_dwordx2 v[252:253], v[6:7], off offset:1152
	v_add_co_u32_e32 v4, vcc, s74, v2
	s_waitcnt vmcnt(0)
	v_cvt_pk_f32_fp8_e32 v[192:193], v188
	v_addc_co_u32_e32 v5, vcc, 0, v3, vcc
	v_mov_b64_e32 v[176:177], v[206:207]
	v_mov_b64_e32 v[174:175], v[208:209]
	v_mov_b64_e32 v[172:173], v[210:211]
	v_mov_b64_e32 v[170:171], v[212:213]
	v_add_co_u32_e32 v6, vcc, s79, v2
	s_nop 1
	v_addc_co_u32_e32 v7, vcc, 0, v3, vcc
	global_load_dwordx2 v[206:207], v[6:7], off nt
	global_load_dwordx2 v[208:209], v[6:7], off offset:1024
	global_load_dwordx2 v[210:211], v[6:7], off offset:128 nt
	global_load_dwordx2 v[212:213], v[6:7], off offset:1152
	v_cvt_pk_f32_fp8_sdwa v[194:195], v188 src0_sel:WORD_1
	v_cvt_pk_f32_fp8_e32 v[196:197], v189
	v_cvt_pk_f32_fp8_sdwa v[188:189], v189 src0_sel:WORD_1
	v_mul_f32_e32 v11, 0xbfb8aa3b, v192
	v_mul_f32_e32 v192, 0xbfb8aa3b, v193
	v_min_f32_e32 v192, 0x42700000, v192
	v_exp_f32_e32 v198, v192
	v_mul_f32_e32 v192, 0xbfb8aa3b, v194
	v_min_f32_e32 v192, 0x42700000, v192
	v_exp_f32_e32 v199, v192
	v_mul_f32_e32 v192, 0xbfb8aa3b, v195
	v_mul_f32_e32 v188, 0xbfb8aa3b, v188
	v_min_f32_e32 v192, 0x42700000, v192
	v_min_f32_e32 v188, 0x42700000, v188
	v_exp_f32_e32 v200, v192
	v_mul_f32_e32 v192, 0xbfb8aa3b, v196
	v_exp_f32_e32 v203, v188
	v_mul_f32_e32 v188, 0xbfb8aa3b, v189
	v_min_f32_e32 v192, 0x42700000, v192
	v_min_f32_e32 v188, 0x42700000, v188
	v_min_f32_e32 v11, 0x42700000, v11
	v_exp_f32_e32 v201, v192
	v_mul_f32_e32 v192, 0xbfb8aa3b, v197
	v_exp_f32_e32 v204, v188
	v_cvt_pk_f32_fp8_e32 v[188:189], v190
	v_exp_f32_e32 v11, v11
	v_min_f32_e32 v192, 0x42700000, v192
	v_exp_f32_e32 v202, v192
	v_cvt_pk_f32_fp8_sdwa v[192:193], v190 src0_sel:WORD_1
	v_mul_f32_e32 v188, 0xbfb8aa3b, v188
	v_mul_f32_e32 v189, 0xbfb8aa3b, v189
	v_min_f32_e32 v188, 0x42700000, v188
	v_min_f32_e32 v189, 0x42700000, v189
	v_add_f32_e32 v11, 1.0, v11
	v_cvt_pk_f32_fp8_e32 v[194:195], v191
	v_exp_f32_e32 v188, v188
	v_exp_f32_e32 v189, v189
	v_mul_f32_e32 v192, 0xbfb8aa3b, v192
	v_mul_f32_e32 v193, 0xbfb8aa3b, v193
	v_rcp_f32_e32 v196, v11
	v_add_f32_e32 v11, 1.0, v198
	v_min_f32_e32 v192, 0x42700000, v192
	v_min_f32_e32 v193, 0x42700000, v193
	v_rcp_f32_e32 v197, v11
	v_add_f32_e32 v11, 1.0, v199
	v_cvt_pk_f32_fp8_sdwa v[190:191], v191 src0_sel:WORD_1
	v_exp_f32_e32 v192, v192
	v_exp_f32_e32 v193, v193
	v_rcp_f32_e32 v198, v11
	v_add_f32_e32 v11, 1.0, v200
	v_rcp_f32_e32 v199, v11
	v_mul_f32_e32 v194, 0xbfb8aa3b, v194
	v_mul_f32_e32 v195, 0xbfb8aa3b, v195
	v_pk_add_f32 v[188:189], v[188:189], 1.0 op_sel_hi:[1,0]
	v_min_f32_e32 v194, 0x42700000, v194
	v_min_f32_e32 v195, 0x42700000, v195
	v_pk_mul_f32 v[188:189], v[196:197], v[188:189]
	v_add_f32_e32 v11, 1.0, v201
	v_exp_f32_e32 v194, v194
	v_exp_f32_e32 v195, v195
	v_mul_f32_e32 v190, 0xbfb8aa3b, v190
	v_mul_f32_e32 v191, 0xbfb8aa3b, v191
	v_pk_add_f32 v[192:193], v[192:193], 1.0 op_sel_hi:[1,0]
	v_pk_mul_f32 v[136:137], v[136:137], v[188:189]
	v_rcp_f32_e32 v188, v11
	v_add_f32_e32 v11, 1.0, v202
	v_min_f32_e32 v190, 0x42700000, v190
	v_min_f32_e32 v191, 0x42700000, v191
	v_pk_mul_f32 v[192:193], v[198:199], v[192:193]
	v_rcp_f32_e32 v189, v11
	v_add_f32_e32 v11, 1.0, v203
	v_exp_f32_e32 v190, v190
	v_exp_f32_e32 v191, v191
	v_pk_mul_f32 v[138:139], v[138:139], v[192:193]
	v_rcp_f32_e32 v192, v11
	v_add_f32_e32 v11, 1.0, v204
	v_rcp_f32_e32 v193, v11
	v_pk_add_f32 v[194:195], v[194:195], 1.0 op_sel_hi:[1,0]
	v_pk_add_f32 v[190:191], v[190:191], 1.0 op_sel_hi:[1,0]
	v_pk_mul_f32 v[188:189], v[188:189], v[194:195]
	v_pk_mul_f32 v[190:191], v[192:193], v[190:191]
	v_pk_mul_f32 v[132:133], v[132:133], v[188:189]
	v_cvt_pk_f32_fp8_e32 v[188:189], v180
	v_pk_mul_f32 v[134:135], v[134:135], v[190:191]
	v_cvt_pk_f32_fp8_sdwa v[190:191], v180 src0_sel:WORD_1
	v_cvt_pk_f32_fp8_e32 v[192:193], v181
	v_cvt_pk_f32_fp8_sdwa v[180:181], v181 src0_sel:WORD_1
	v_mul_f32_e32 v11, 0xbfb8aa3b, v188
	v_mul_f32_e32 v188, 0xbfb8aa3b, v189
	v_min_f32_e32 v188, 0x42700000, v188
	v_exp_f32_e32 v194, v188
	v_mul_f32_e32 v188, 0xbfb8aa3b, v190
	v_min_f32_e32 v188, 0x42700000, v188
	v_exp_f32_e32 v195, v188
	v_mul_f32_e32 v188, 0xbfb8aa3b, v191
	v_mul_f32_e32 v180, 0xbfb8aa3b, v180
	v_min_f32_e32 v188, 0x42700000, v188
	v_min_f32_e32 v180, 0x42700000, v180
	v_exp_f32_e32 v196, v188
	v_mul_f32_e32 v188, 0xbfb8aa3b, v192
	v_exp_f32_e32 v199, v180
	v_mul_f32_e32 v180, 0xbfb8aa3b, v181
	v_min_f32_e32 v188, 0x42700000, v188
	v_min_f32_e32 v180, 0x42700000, v180
	v_min_f32_e32 v11, 0x42700000, v11
	v_exp_f32_e32 v197, v188
	v_mul_f32_e32 v188, 0xbfb8aa3b, v193
	v_exp_f32_e32 v200, v180
	v_cvt_pk_f32_fp8_e32 v[180:181], v178
	v_exp_f32_e32 v11, v11
	v_min_f32_e32 v188, 0x42700000, v188
	v_exp_f32_e32 v198, v188
	v_cvt_pk_f32_fp8_sdwa v[188:189], v178 src0_sel:WORD_1
	v_mul_f32_e32 v180, 0xbfb8aa3b, v180
	v_mul_f32_e32 v181, 0xbfb8aa3b, v181
	v_add_co_u32_e32 v4, vcc, s61, v2
	v_min_f32_e32 v180, 0x42700000, v180
	v_min_f32_e32 v181, 0x42700000, v181
	v_add_f32_e32 v11, 1.0, v11
	v_addc_co_u32_e32 v5, vcc, 0, v3, vcc
	v_exp_f32_e32 v180, v180
	v_exp_f32_e32 v181, v181
	v_mul_f32_e32 v188, 0xbfb8aa3b, v188
	v_mul_f32_e32 v189, 0xbfb8aa3b, v189
	v_rcp_f32_e32 v192, v11
	v_add_f32_e32 v11, 1.0, v194
	v_mov_b64_e32 v[168:169], v[214:215]
	v_mov_b64_e32 v[166:167], v[216:217]
	v_mov_b64_e32 v[164:165], v[218:219]
	v_mov_b64_e32 v[162:163], v[220:221]
	v_min_f32_e32 v188, 0x42700000, v188
	v_min_f32_e32 v189, 0x42700000, v189
	v_rcp_f32_e32 v193, v11
	v_add_f32_e32 v11, 1.0, v195
	v_cvt_pk_f32_fp8_e32 v[190:191], v179
	v_cvt_pk_f32_fp8_sdwa v[178:179], v179 src0_sel:WORD_1
	v_exp_f32_e32 v188, v188
	v_exp_f32_e32 v189, v189
	v_rcp_f32_e32 v194, v11
	v_add_f32_e32 v11, 1.0, v196
	v_rcp_f32_e32 v195, v11
	v_pk_add_f32 v[180:181], v[180:181], 1.0 op_sel_hi:[1,0]
	v_add_f32_e32 v11, 1.0, v197
	v_pk_mul_f32 v[180:181], v[192:193], v[180:181]
	v_mul_f32_e32 v178, 0xbfb8aa3b, v178
	v_mul_f32_e32 v179, 0xbfb8aa3b, v179
	v_pk_add_f32 v[188:189], v[188:189], 1.0 op_sel_hi:[1,0]
	v_pk_mul_f32 v[128:129], v[128:129], v[180:181]
	v_rcp_f32_e32 v180, v11
	v_add_f32_e32 v11, 1.0, v198
	v_min_f32_e32 v178, 0x42700000, v178
	v_min_f32_e32 v179, 0x42700000, v179
	v_pk_mul_f32 v[188:189], v[194:195], v[188:189]
	v_rcp_f32_e32 v181, v11
	v_add_f32_e32 v11, 1.0, v199
	v_mul_f32_e32 v190, 0xbfb8aa3b, v190
	v_mul_f32_e32 v191, 0xbfb8aa3b, v191
	v_exp_f32_e32 v178, v178
	v_exp_f32_e32 v179, v179
	v_pk_mul_f32 v[130:131], v[130:131], v[188:189]
	v_rcp_f32_e32 v188, v11
	v_add_f32_e32 v11, 1.0, v200
	v_min_f32_e32 v190, 0x42700000, v190
	v_min_f32_e32 v191, 0x42700000, v191
	v_rcp_f32_e32 v189, v11
	v_exp_f32_e32 v190, v190
	v_exp_f32_e32 v191, v191
	v_pk_add_f32 v[178:179], v[178:179], 1.0 op_sel_hi:[1,0]
	v_add_co_u32_e32 v4, vcc, s73, v2
	v_pk_mul_f32 v[178:179], v[188:189], v[178:179]
	v_pk_add_f32 v[190:191], v[190:191], 1.0 op_sel_hi:[1,0]
	v_pk_mul_f32 v[126:127], v[126:127], v[178:179]
	s_waitcnt vmcnt(0)
	v_cvt_pk_f32_fp8_e32 v[178:179], v176
	v_pk_mul_f32 v[180:181], v[180:181], v[190:191]
	v_cvt_pk_f32_fp8_e32 v[188:189], v177
	v_pk_mul_f32 v[124:125], v[124:125], v[180:181]
	v_cvt_pk_f32_fp8_sdwa v[180:181], v176 src0_sel:WORD_1
	v_cvt_pk_f32_fp8_sdwa v[176:177], v177 src0_sel:WORD_1
	v_mul_f32_e32 v11, 0xbfb8aa3b, v178
	v_mul_f32_e32 v178, 0xbfb8aa3b, v179
	v_min_f32_e32 v178, 0x42700000, v178
	v_exp_f32_e32 v190, v178
	v_mul_f32_e32 v178, 0xbfb8aa3b, v180
	v_min_f32_e32 v178, 0x42700000, v178
	v_exp_f32_e32 v191, v178
	v_mul_f32_e32 v178, 0xbfb8aa3b, v181
	v_mul_f32_e32 v176, 0xbfb8aa3b, v176
	v_min_f32_e32 v178, 0x42700000, v178
	v_min_f32_e32 v176, 0x42700000, v176
	v_exp_f32_e32 v192, v178
	v_mul_f32_e32 v178, 0xbfb8aa3b, v188
	v_exp_f32_e32 v195, v176
	v_mul_f32_e32 v176, 0xbfb8aa3b, v177
	v_min_f32_e32 v178, 0x42700000, v178
	v_min_f32_e32 v176, 0x42700000, v176
	v_min_f32_e32 v11, 0x42700000, v11
	v_exp_f32_e32 v193, v178
	v_mul_f32_e32 v178, 0xbfb8aa3b, v189
	v_exp_f32_e32 v196, v176
	v_cvt_pk_f32_fp8_e32 v[176:177], v174
	v_exp_f32_e32 v11, v11
	v_min_f32_e32 v178, 0x42700000, v178
	v_exp_f32_e32 v194, v178
	v_cvt_pk_f32_fp8_sdwa v[178:179], v174 src0_sel:WORD_1
	v_mul_f32_e32 v176, 0xbfb8aa3b, v176
	v_mul_f32_e32 v177, 0xbfb8aa3b, v177
	v_min_f32_e32 v176, 0x42700000, v176
	v_min_f32_e32 v177, 0x42700000, v177
	v_add_f32_e32 v11, 1.0, v11
	v_exp_f32_e32 v176, v176
	v_exp_f32_e32 v177, v177
	v_mul_f32_e32 v178, 0xbfb8aa3b, v178
	v_mul_f32_e32 v179, 0xbfb8aa3b, v179
	v_rcp_f32_e32 v188, v11
	v_add_f32_e32 v11, 1.0, v190
	v_min_f32_e32 v178, 0x42700000, v178
	v_min_f32_e32 v179, 0x42700000, v179
	v_rcp_f32_e32 v189, v11
	v_add_f32_e32 v11, 1.0, v191
	v_cvt_pk_f32_fp8_e32 v[180:181], v175
	v_cvt_pk_f32_fp8_sdwa v[174:175], v175 src0_sel:WORD_1
	v_exp_f32_e32 v178, v178
	v_exp_f32_e32 v179, v179
	v_rcp_f32_e32 v190, v11
	v_add_f32_e32 v11, 1.0, v192
	v_rcp_f32_e32 v191, v11
	v_pk_add_f32 v[176:177], v[176:177], 1.0 op_sel_hi:[1,0]
	v_add_f32_e32 v11, 1.0, v193
	v_pk_mul_f32 v[176:177], v[188:189], v[176:177]
	v_mul_f32_e32 v174, 0xbfb8aa3b, v174
	v_mul_f32_e32 v175, 0xbfb8aa3b, v175
	v_pk_add_f32 v[178:179], v[178:179], 1.0 op_sel_hi:[1,0]
	v_pk_mul_f32 v[120:121], v[120:121], v[176:177]
	v_rcp_f32_e32 v176, v11
	v_add_f32_e32 v11, 1.0, v194
	v_min_f32_e32 v174, 0x42700000, v174
	v_min_f32_e32 v175, 0x42700000, v175
	v_pk_mul_f32 v[178:179], v[190:191], v[178:179]
	v_rcp_f32_e32 v177, v11
	v_add_f32_e32 v11, 1.0, v195
	v_mul_f32_e32 v180, 0xbfb8aa3b, v180
	v_mul_f32_e32 v181, 0xbfb8aa3b, v181
	v_exp_f32_e32 v174, v174
	v_exp_f32_e32 v175, v175
	v_pk_mul_f32 v[122:123], v[122:123], v[178:179]
	v_rcp_f32_e32 v178, v11
	v_add_f32_e32 v11, 1.0, v196
	v_min_f32_e32 v180, 0x42700000, v180
	v_min_f32_e32 v181, 0x42700000, v181
	v_rcp_f32_e32 v179, v11
	v_exp_f32_e32 v180, v180
	v_exp_f32_e32 v181, v181
	v_pk_add_f32 v[174:175], v[174:175], 1.0 op_sel_hi:[1,0]
	v_addc_co_u32_e32 v5, vcc, 0, v3, vcc
	v_pk_mul_f32 v[174:175], v[178:179], v[174:175]
	v_pk_add_f32 v[180:181], v[180:181], 1.0 op_sel_hi:[1,0]
	v_pk_mul_f32 v[118:119], v[118:119], v[174:175]
	v_cvt_pk_f32_fp8_e32 v[174:175], v172
	v_pk_mul_f32 v[176:177], v[176:177], v[180:181]
	v_cvt_pk_f32_fp8_e32 v[178:179], v173
	v_pk_mul_f32 v[116:117], v[116:117], v[176:177]
	v_cvt_pk_f32_fp8_sdwa v[176:177], v172 src0_sel:WORD_1
	v_cvt_pk_f32_fp8_sdwa v[172:173], v173 src0_sel:WORD_1
	v_mul_f32_e32 v11, 0xbfb8aa3b, v174
	v_mul_f32_e32 v174, 0xbfb8aa3b, v175
	v_min_f32_e32 v174, 0x42700000, v174
	v_exp_f32_e32 v180, v174
	v_mul_f32_e32 v174, 0xbfb8aa3b, v176
	v_min_f32_e32 v174, 0x42700000, v174
	v_exp_f32_e32 v181, v174
	v_mul_f32_e32 v174, 0xbfb8aa3b, v177
	v_mul_f32_e32 v172, 0xbfb8aa3b, v172
	v_min_f32_e32 v174, 0x42700000, v174
	v_min_f32_e32 v172, 0x42700000, v172
	v_exp_f32_e32 v188, v174
	v_mul_f32_e32 v174, 0xbfb8aa3b, v178
	v_exp_f32_e32 v191, v172
	v_mul_f32_e32 v172, 0xbfb8aa3b, v173
	v_min_f32_e32 v174, 0x42700000, v174
	v_min_f32_e32 v172, 0x42700000, v172
	v_min_f32_e32 v11, 0x42700000, v11
	v_exp_f32_e32 v189, v174
	v_mul_f32_e32 v174, 0xbfb8aa3b, v179
	v_exp_f32_e32 v192, v172
	v_cvt_pk_f32_fp8_e32 v[172:173], v170
	v_exp_f32_e32 v11, v11
	v_min_f32_e32 v174, 0x42700000, v174
	v_exp_f32_e32 v190, v174
	v_cvt_pk_f32_fp8_sdwa v[174:175], v170 src0_sel:WORD_1
	v_mul_f32_e32 v172, 0xbfb8aa3b, v172
	v_mul_f32_e32 v173, 0xbfb8aa3b, v173
	v_min_f32_e32 v172, 0x42700000, v172
	v_min_f32_e32 v173, 0x42700000, v173
	v_add_f32_e32 v11, 1.0, v11
	v_exp_f32_e32 v172, v172
	v_exp_f32_e32 v173, v173
	v_mul_f32_e32 v174, 0xbfb8aa3b, v174
	v_mul_f32_e32 v175, 0xbfb8aa3b, v175
	v_rcp_f32_e32 v178, v11
	v_add_f32_e32 v11, 1.0, v180
	v_mov_b64_e32 v[160:161], v[222:223]
	v_mov_b64_e32 v[8:9], v[224:225]
	v_mov_b64_e32 v[6:7], v[226:227]
	s_nop 0
	v_mov_b64_e32 v[4:5], v[228:229]
	v_min_f32_e32 v174, 0x42700000, v174
	v_min_f32_e32 v175, 0x42700000, v175
	v_rcp_f32_e32 v179, v11
	v_add_f32_e32 v11, 1.0, v181
	v_cvt_pk_f32_fp8_e32 v[176:177], v171
	v_cvt_pk_f32_fp8_sdwa v[170:171], v171 src0_sel:WORD_1
	v_exp_f32_e32 v174, v174
	v_exp_f32_e32 v175, v175
	v_rcp_f32_e32 v180, v11
	v_add_f32_e32 v11, 1.0, v188
	v_rcp_f32_e32 v181, v11
	v_pk_add_f32 v[172:173], v[172:173], 1.0 op_sel_hi:[1,0]
	v_add_f32_e32 v11, 1.0, v189
	v_pk_mul_f32 v[172:173], v[178:179], v[172:173]
	v_mul_f32_e32 v170, 0xbfb8aa3b, v170
	v_mul_f32_e32 v171, 0xbfb8aa3b, v171
	v_pk_add_f32 v[174:175], v[174:175], 1.0 op_sel_hi:[1,0]
	v_pk_mul_f32 v[112:113], v[112:113], v[172:173]
	v_rcp_f32_e32 v172, v11
	v_add_f32_e32 v11, 1.0, v190
	v_min_f32_e32 v170, 0x42700000, v170
	v_min_f32_e32 v171, 0x42700000, v171
	v_pk_mul_f32 v[174:175], v[180:181], v[174:175]
	v_rcp_f32_e32 v173, v11
	v_add_f32_e32 v11, 1.0, v191
	v_mul_f32_e32 v176, 0xbfb8aa3b, v176
	v_mul_f32_e32 v177, 0xbfb8aa3b, v177
	v_exp_f32_e32 v170, v170
	v_exp_f32_e32 v171, v171
	v_pk_mul_f32 v[114:115], v[114:115], v[174:175]
	v_rcp_f32_e32 v174, v11
	v_add_f32_e32 v11, 1.0, v192
	v_min_f32_e32 v176, 0x42700000, v176
	v_min_f32_e32 v177, 0x42700000, v177
	v_rcp_f32_e32 v175, v11
	v_exp_f32_e32 v176, v176
	v_exp_f32_e32 v177, v177
	v_pk_add_f32 v[170:171], v[170:171], 1.0 op_sel_hi:[1,0]
	v_pk_add_f32 v[176:177], v[176:177], 1.0 op_sel_hi:[1,0]
	v_pk_mul_f32 v[170:171], v[174:175], v[170:171]
	v_pk_mul_f32 v[172:173], v[172:173], v[176:177]
	v_pk_mul_f32 v[110:111], v[110:111], v[170:171]
	v_cvt_pk_f32_fp8_e32 v[170:171], v168
	v_pk_mul_f32 v[108:109], v[108:109], v[172:173]
	v_cvt_pk_f32_fp8_sdwa v[172:173], v168 src0_sel:WORD_1
	v_cvt_pk_f32_fp8_e32 v[174:175], v169
	v_cvt_pk_f32_fp8_sdwa v[168:169], v169 src0_sel:WORD_1
	v_mul_f32_e32 v11, 0xbfb8aa3b, v170
	v_mul_f32_e32 v170, 0xbfb8aa3b, v171
	v_min_f32_e32 v170, 0x42700000, v170
	v_exp_f32_e32 v176, v170
	v_mul_f32_e32 v170, 0xbfb8aa3b, v172
	v_min_f32_e32 v170, 0x42700000, v170
	v_exp_f32_e32 v177, v170
	v_mul_f32_e32 v170, 0xbfb8aa3b, v173
	v_mul_f32_e32 v168, 0xbfb8aa3b, v168
	v_min_f32_e32 v170, 0x42700000, v170
	v_min_f32_e32 v168, 0x42700000, v168
	v_exp_f32_e32 v178, v170
	v_mul_f32_e32 v170, 0xbfb8aa3b, v174
	v_exp_f32_e32 v181, v168
	v_mul_f32_e32 v168, 0xbfb8aa3b, v169
	v_min_f32_e32 v170, 0x42700000, v170
	v_min_f32_e32 v168, 0x42700000, v168
	v_min_f32_e32 v11, 0x42700000, v11
	v_exp_f32_e32 v179, v170
	v_mul_f32_e32 v170, 0xbfb8aa3b, v175
	v_exp_f32_e32 v188, v168
	v_cvt_pk_f32_fp8_e32 v[168:169], v166
	v_exp_f32_e32 v11, v11
	v_min_f32_e32 v170, 0x42700000, v170
	v_exp_f32_e32 v180, v170
	v_cvt_pk_f32_fp8_sdwa v[170:171], v166 src0_sel:WORD_1
	v_mul_f32_e32 v168, 0xbfb8aa3b, v168
	v_mul_f32_e32 v169, 0xbfb8aa3b, v169
	v_min_f32_e32 v168, 0x42700000, v168
	v_min_f32_e32 v169, 0x42700000, v169
	v_add_f32_e32 v11, 1.0, v11
	v_exp_f32_e32 v168, v168
	v_exp_f32_e32 v169, v169
	v_mul_f32_e32 v170, 0xbfb8aa3b, v170
	v_mul_f32_e32 v171, 0xbfb8aa3b, v171
	v_rcp_f32_e32 v174, v11
	v_add_f32_e32 v11, 1.0, v176
	v_min_f32_e32 v170, 0x42700000, v170
	v_min_f32_e32 v171, 0x42700000, v171
	v_rcp_f32_e32 v175, v11
	v_add_f32_e32 v11, 1.0, v177
	v_cvt_pk_f32_fp8_e32 v[172:173], v167
	v_cvt_pk_f32_fp8_sdwa v[166:167], v167 src0_sel:WORD_1
	v_exp_f32_e32 v170, v170
	v_exp_f32_e32 v171, v171
	v_rcp_f32_e32 v176, v11
	v_add_f32_e32 v11, 1.0, v178
	v_rcp_f32_e32 v177, v11
	v_pk_add_f32 v[168:169], v[168:169], 1.0 op_sel_hi:[1,0]
	v_add_f32_e32 v11, 1.0, v179
	v_pk_mul_f32 v[168:169], v[174:175], v[168:169]
	v_mul_f32_e32 v166, 0xbfb8aa3b, v166
	v_mul_f32_e32 v167, 0xbfb8aa3b, v167
	v_pk_add_f32 v[170:171], v[170:171], 1.0 op_sel_hi:[1,0]
	v_pk_mul_f32 v[104:105], v[104:105], v[168:169]
	v_rcp_f32_e32 v168, v11
	v_add_f32_e32 v11, 1.0, v180
	v_min_f32_e32 v166, 0x42700000, v166
	v_min_f32_e32 v167, 0x42700000, v167
	v_pk_mul_f32 v[170:171], v[176:177], v[170:171]
	v_rcp_f32_e32 v169, v11
	v_add_f32_e32 v11, 1.0, v181
	v_mul_f32_e32 v172, 0xbfb8aa3b, v172
	v_mul_f32_e32 v173, 0xbfb8aa3b, v173
	v_exp_f32_e32 v166, v166
	v_exp_f32_e32 v167, v167
	v_pk_mul_f32 v[106:107], v[106:107], v[170:171]
	v_rcp_f32_e32 v170, v11
	v_add_f32_e32 v11, 1.0, v188
	v_min_f32_e32 v172, 0x42700000, v172
	v_min_f32_e32 v173, 0x42700000, v173
	v_rcp_f32_e32 v171, v11
	v_exp_f32_e32 v172, v172
	v_exp_f32_e32 v173, v173
	v_pk_add_f32 v[166:167], v[166:167], 1.0 op_sel_hi:[1,0]
	v_pk_add_f32 v[172:173], v[172:173], 1.0 op_sel_hi:[1,0]
	v_pk_mul_f32 v[166:167], v[170:171], v[166:167]
	v_pk_mul_f32 v[168:169], v[168:169], v[172:173]
	v_pk_mul_f32 v[102:103], v[102:103], v[166:167]
	v_cvt_pk_f32_fp8_e32 v[166:167], v164
	v_pk_mul_f32 v[100:101], v[100:101], v[168:169]
	v_cvt_pk_f32_fp8_sdwa v[168:169], v164 src0_sel:WORD_1
	v_cvt_pk_f32_fp8_e32 v[170:171], v165
	v_cvt_pk_f32_fp8_sdwa v[164:165], v165 src0_sel:WORD_1
	v_mul_f32_e32 v11, 0xbfb8aa3b, v166
	v_mul_f32_e32 v166, 0xbfb8aa3b, v167
	v_min_f32_e32 v166, 0x42700000, v166
	v_exp_f32_e32 v172, v166
	v_mul_f32_e32 v166, 0xbfb8aa3b, v168
	v_min_f32_e32 v166, 0x42700000, v166
	v_exp_f32_e32 v173, v166
	v_mul_f32_e32 v166, 0xbfb8aa3b, v169
	v_mul_f32_e32 v164, 0xbfb8aa3b, v164
	v_min_f32_e32 v166, 0x42700000, v166
	v_min_f32_e32 v164, 0x42700000, v164
	v_exp_f32_e32 v174, v166
	v_mul_f32_e32 v166, 0xbfb8aa3b, v170
	v_exp_f32_e32 v177, v164
	v_mul_f32_e32 v164, 0xbfb8aa3b, v165
	v_min_f32_e32 v166, 0x42700000, v166
	v_min_f32_e32 v164, 0x42700000, v164
	v_min_f32_e32 v11, 0x42700000, v11
	v_exp_f32_e32 v175, v166
	v_mul_f32_e32 v166, 0xbfb8aa3b, v171
	v_exp_f32_e32 v178, v164
	v_cvt_pk_f32_fp8_e32 v[164:165], v162
	v_exp_f32_e32 v11, v11
	v_min_f32_e32 v166, 0x42700000, v166
	v_exp_f32_e32 v176, v166
	v_cvt_pk_f32_fp8_sdwa v[166:167], v162 src0_sel:WORD_1
	v_mul_f32_e32 v164, 0xbfb8aa3b, v164
	v_mul_f32_e32 v165, 0xbfb8aa3b, v165
	v_min_f32_e32 v164, 0x42700000, v164
	v_min_f32_e32 v165, 0x42700000, v165
	v_add_f32_e32 v11, 1.0, v11
	v_exp_f32_e32 v164, v164
	v_exp_f32_e32 v165, v165
	v_mul_f32_e32 v166, 0xbfb8aa3b, v166
	v_mul_f32_e32 v167, 0xbfb8aa3b, v167
	v_rcp_f32_e32 v170, v11
	v_add_f32_e32 v11, 1.0, v172
	v_min_f32_e32 v166, 0x42700000, v166
	v_min_f32_e32 v167, 0x42700000, v167
	v_rcp_f32_e32 v171, v11
	v_add_f32_e32 v11, 1.0, v173
	v_cvt_pk_f32_fp8_e32 v[168:169], v163
	v_cvt_pk_f32_fp8_sdwa v[162:163], v163 src0_sel:WORD_1
	v_exp_f32_e32 v166, v166
	v_exp_f32_e32 v167, v167
	v_rcp_f32_e32 v172, v11
	v_add_f32_e32 v11, 1.0, v174
	v_rcp_f32_e32 v173, v11
	v_pk_add_f32 v[164:165], v[164:165], 1.0 op_sel_hi:[1,0]
	v_add_f32_e32 v11, 1.0, v175
	v_pk_mul_f32 v[164:165], v[170:171], v[164:165]
	v_mul_f32_e32 v162, 0xbfb8aa3b, v162
	v_mul_f32_e32 v163, 0xbfb8aa3b, v163
	v_pk_add_f32 v[166:167], v[166:167], 1.0 op_sel_hi:[1,0]
	v_pk_mul_f32 v[96:97], v[96:97], v[164:165]
	v_rcp_f32_e32 v164, v11
	v_add_f32_e32 v11, 1.0, v176
	v_min_f32_e32 v162, 0x42700000, v162
	v_min_f32_e32 v163, 0x42700000, v163
	v_pk_mul_f32 v[166:167], v[172:173], v[166:167]
	v_rcp_f32_e32 v165, v11
	v_add_f32_e32 v11, 1.0, v177
	v_mul_f32_e32 v168, 0xbfb8aa3b, v168
	v_mul_f32_e32 v169, 0xbfb8aa3b, v169
	v_exp_f32_e32 v162, v162
	v_exp_f32_e32 v163, v163
	v_pk_mul_f32 v[98:99], v[98:99], v[166:167]
	v_rcp_f32_e32 v166, v11
	v_add_f32_e32 v11, 1.0, v178
	v_min_f32_e32 v168, 0x42700000, v168
	v_min_f32_e32 v169, 0x42700000, v169
	v_rcp_f32_e32 v167, v11
	v_exp_f32_e32 v168, v168
	v_exp_f32_e32 v169, v169
	v_pk_add_f32 v[162:163], v[162:163], 1.0 op_sel_hi:[1,0]
	v_pk_add_f32 v[168:169], v[168:169], 1.0 op_sel_hi:[1,0]
	v_pk_mul_f32 v[162:163], v[166:167], v[162:163]
	v_pk_mul_f32 v[164:165], v[164:165], v[168:169]
	v_pk_mul_f32 v[94:95], v[94:95], v[162:163]
	s_waitcnt vmcnt(0)
	v_cvt_pk_f32_fp8_e32 v[162:163], v160
	v_pk_mul_f32 v[92:93], v[92:93], v[164:165]
	v_cvt_pk_f32_fp8_sdwa v[164:165], v160 src0_sel:WORD_1
	v_cvt_pk_f32_fp8_e32 v[166:167], v161
	v_cvt_pk_f32_fp8_sdwa v[160:161], v161 src0_sel:WORD_1
	v_mul_f32_e32 v11, 0xbfb8aa3b, v162
	v_mul_f32_e32 v162, 0xbfb8aa3b, v163
	v_min_f32_e32 v162, 0x42700000, v162
	v_exp_f32_e32 v168, v162
	v_mul_f32_e32 v162, 0xbfb8aa3b, v164
	v_min_f32_e32 v162, 0x42700000, v162
	v_exp_f32_e32 v169, v162
	v_mul_f32_e32 v162, 0xbfb8aa3b, v165
	v_mul_f32_e32 v160, 0xbfb8aa3b, v160
	v_min_f32_e32 v162, 0x42700000, v162
	v_min_f32_e32 v160, 0x42700000, v160
	v_exp_f32_e32 v170, v162
	v_mul_f32_e32 v162, 0xbfb8aa3b, v166
	v_exp_f32_e32 v173, v160
	v_mul_f32_e32 v160, 0xbfb8aa3b, v161
	v_min_f32_e32 v162, 0x42700000, v162
	v_min_f32_e32 v160, 0x42700000, v160
	v_min_f32_e32 v11, 0x42700000, v11
	v_exp_f32_e32 v171, v162
	v_mul_f32_e32 v162, 0xbfb8aa3b, v167
	v_exp_f32_e32 v174, v160
	v_cvt_pk_f32_fp8_e32 v[160:161], v8
	v_exp_f32_e32 v11, v11
	v_min_f32_e32 v162, 0x42700000, v162
	v_exp_f32_e32 v172, v162
	v_cvt_pk_f32_fp8_sdwa v[162:163], v8 src0_sel:WORD_1
	v_mul_f32_e32 v160, 0xbfb8aa3b, v160
	v_mul_f32_e32 v161, 0xbfb8aa3b, v161
	v_min_f32_e32 v160, 0x42700000, v160
	v_min_f32_e32 v161, 0x42700000, v161
	v_add_f32_e32 v11, 1.0, v11
	v_exp_f32_e32 v160, v160
	v_exp_f32_e32 v161, v161
	v_mul_f32_e32 v162, 0xbfb8aa3b, v162
	v_mul_f32_e32 v163, 0xbfb8aa3b, v163
	v_rcp_f32_e32 v166, v11
	v_add_f32_e32 v11, 1.0, v168
	v_min_f32_e32 v162, 0x42700000, v162
	v_min_f32_e32 v163, 0x42700000, v163
	v_rcp_f32_e32 v167, v11
	v_add_f32_e32 v11, 1.0, v169
	v_cvt_pk_f32_fp8_e32 v[164:165], v9
	v_cvt_pk_f32_fp8_sdwa v[8:9], v9 src0_sel:WORD_1
	v_exp_f32_e32 v162, v162
	v_exp_f32_e32 v163, v163
	v_rcp_f32_e32 v168, v11
	v_add_f32_e32 v11, 1.0, v170
	v_rcp_f32_e32 v169, v11
	v_pk_add_f32 v[160:161], v[160:161], 1.0 op_sel_hi:[1,0]
	v_add_f32_e32 v11, 1.0, v171
	v_pk_mul_f32 v[160:161], v[166:167], v[160:161]
	v_mul_f32_e32 v8, 0xbfb8aa3b, v8
	v_mul_f32_e32 v9, 0xbfb8aa3b, v9
	v_pk_add_f32 v[162:163], v[162:163], 1.0 op_sel_hi:[1,0]
	v_pk_mul_f32 v[88:89], v[88:89], v[160:161]
	v_rcp_f32_e32 v160, v11
	v_add_f32_e32 v11, 1.0, v172
	v_min_f32_e32 v8, 0x42700000, v8
	v_min_f32_e32 v9, 0x42700000, v9
	v_pk_mul_f32 v[162:163], v[168:169], v[162:163]
	v_rcp_f32_e32 v161, v11
	v_add_f32_e32 v11, 1.0, v173
	v_exp_f32_e32 v8, v8
	v_exp_f32_e32 v9, v9
	v_pk_mul_f32 v[90:91], v[90:91], v[162:163]
	v_rcp_f32_e32 v162, v11
	v_add_f32_e32 v11, 1.0, v174
	v_rcp_f32_e32 v163, v11
	v_mul_f32_e32 v164, 0xbfb8aa3b, v164
	v_mul_f32_e32 v165, 0xbfb8aa3b, v165
	v_min_f32_e32 v164, 0x42700000, v164
	v_min_f32_e32 v165, 0x42700000, v165
	v_exp_f32_e32 v164, v164
	v_exp_f32_e32 v165, v165
	v_pk_add_f32 v[8:9], v[8:9], 1.0 op_sel_hi:[1,0]
	v_pk_add_f32 v[164:165], v[164:165], 1.0 op_sel_hi:[1,0]
	v_pk_mul_f32 v[8:9], v[162:163], v[8:9]
	v_pk_mul_f32 v[160:161], v[160:161], v[164:165]
	v_pk_mul_f32 v[86:87], v[86:87], v[8:9]
	v_cvt_pk_f32_fp8_e32 v[8:9], v6
	v_pk_mul_f32 v[84:85], v[84:85], v[160:161]
	v_cvt_pk_f32_fp8_sdwa v[160:161], v6 src0_sel:WORD_1
	v_cvt_pk_f32_fp8_e32 v[162:163], v7
	v_mul_f32_e32 v8, 0xbfb8aa3b, v8
	v_min_f32_e32 v8, 0x42700000, v8
	v_exp_f32_e32 v11, v8
	v_mul_f32_e32 v8, 0xbfb8aa3b, v9
	v_min_f32_e32 v8, 0x42700000, v8
	v_exp_f32_e32 v164, v8
	v_mul_f32_e32 v8, 0xbfb8aa3b, v160
	v_min_f32_e32 v8, 0x42700000, v8
	v_exp_f32_e32 v165, v8
	v_mul_f32_e32 v8, 0xbfb8aa3b, v161
	v_min_f32_e32 v8, 0x42700000, v8
	v_exp_f32_e32 v166, v8
	v_mul_f32_e32 v8, 0xbfb8aa3b, v162
	v_min_f32_e32 v8, 0x42700000, v8
	v_cvt_pk_f32_fp8_sdwa v[6:7], v7 src0_sel:WORD_1
	v_exp_f32_e32 v167, v8
	v_mul_f32_e32 v8, 0xbfb8aa3b, v163
	v_min_f32_e32 v8, 0x42700000, v8
	v_exp_f32_e32 v168, v8
	v_cvt_pk_f32_fp8_sdwa v[8:9], v4 src0_sel:WORD_1
	v_mul_f32_e32 v6, 0xbfb8aa3b, v6
	v_min_f32_e32 v6, 0x42700000, v6
	v_add_f32_e32 v11, 1.0, v11
	v_exp_f32_e32 v169, v6
	v_mul_f32_e32 v6, 0xbfb8aa3b, v7
	v_mul_f32_e32 v8, 0xbfb8aa3b, v8
	v_mul_f32_e32 v9, 0xbfb8aa3b, v9
	v_rcp_f32_e32 v162, v11
	v_add_f32_e32 v11, 1.0, v164
	v_min_f32_e32 v6, 0x42700000, v6
	v_min_f32_e32 v8, 0x42700000, v8
	v_min_f32_e32 v9, 0x42700000, v9
	v_rcp_f32_e32 v163, v11
	v_add_f32_e32 v11, 1.0, v165
	v_exp_f32_e32 v170, v6
	v_cvt_pk_f32_fp8_e32 v[6:7], v4
	v_cvt_pk_f32_fp8_e32 v[160:161], v5
	v_cvt_pk_f32_fp8_sdwa v[4:5], v5 src0_sel:WORD_1
	v_exp_f32_e32 v8, v8
	v_exp_f32_e32 v9, v9
	v_rcp_f32_e32 v164, v11
	v_add_f32_e32 v11, 1.0, v166
	v_rcp_f32_e32 v165, v11
	v_mul_f32_e32 v4, 0xbfb8aa3b, v4
	v_mul_f32_e32 v5, 0xbfb8aa3b, v5
	v_pk_add_f32 v[8:9], v[8:9], 1.0 op_sel_hi:[1,0]
	v_min_f32_e32 v4, 0x42700000, v4
	v_min_f32_e32 v5, 0x42700000, v5
	v_pk_mul_f32 v[8:9], v[164:165], v[8:9]
	v_exp_f32_e32 v4, v4
	v_exp_f32_e32 v5, v5
	v_pk_mul_f32 v[82:83], v[82:83], v[8:9]
	v_add_f32_e32 v8, 1.0, v169
	v_add_f32_e32 v9, 1.0, v170
	v_rcp_f32_e32 v8, v8
	v_rcp_f32_e32 v9, v9
	v_pk_add_f32 v[4:5], v[4:5], 1.0 op_sel_hi:[1,0]
	v_mul_f32_e32 v6, 0xbfb8aa3b, v6
	v_mul_f32_e32 v7, 0xbfb8aa3b, v7
	v_pk_mul_f32 v[4:5], v[8:9], v[4:5]
	v_min_f32_e32 v6, 0x42700000, v6
	v_pk_mul_f32 v[78:79], v[78:79], v[4:5]
	v_add_co_u32_e32 v4, vcc, s76, v2
	v_min_f32_e32 v7, 0x42700000, v7
	s_nop 0
	v_addc_co_u32_e32 v5, vcc, 0, v3, vcc
	v_mov_b64_e32 v[174:175], v[230:231]
	v_mov_b64_e32 v[180:181], v[232:233]
	v_mov_b64_e32 v[176:177], v[234:235]
	v_mov_b64_e32 v[188:189], v[236:237]
	v_exp_f32_e32 v6, v6
	v_exp_f32_e32 v7, v7
	v_add_co_u32_e32 v4, vcc, s77, v2
	v_mul_f32_e32 v160, 0xbfb8aa3b, v160
	v_pk_add_f32 v[6:7], v[6:7], 1.0 op_sel_hi:[1,0]
	v_addc_co_u32_e32 v5, vcc, 0, v3, vcc
	v_pk_mul_f32 v[6:7], v[162:163], v[6:7]
	v_mul_f32_e32 v161, 0xbfb8aa3b, v161
	v_pk_mul_f32 v[80:81], v[80:81], v[6:7]
	v_add_f32_e32 v7, 1.0, v168
	v_mov_b64_e32 v[178:179], v[238:239]
	v_mov_b64_e32 v[172:173], v[240:241]
	v_mov_b64_e32 v[170:171], v[242:243]
	v_mov_b64_e32 v[168:169], v[244:245]
	v_min_f32_e32 v160, 0x42700000, v160
	v_min_f32_e32 v161, 0x42700000, v161
	v_exp_f32_e32 v160, v160
	v_exp_f32_e32 v161, v161
	v_add_f32_e32 v6, 1.0, v167
	v_rcp_f32_e32 v6, v6
	v_rcp_f32_e32 v7, v7
	v_add_co_u32_e32 v4, vcc, s78, v2
	v_pk_add_f32 v[160:161], v[160:161], 1.0 op_sel_hi:[1,0]
	s_nop 0
	v_addc_co_u32_e32 v5, vcc, 0, v3, vcc
	v_pk_mul_f32 v[6:7], v[6:7], v[160:161]
	v_mov_b64_e32 v[166:167], v[246:247]
	v_mov_b64_e32 v[164:165], v[248:249]
	v_mov_b64_e32 v[162:163], v[250:251]
	v_mov_b64_e32 v[160:161], v[252:253]
	v_add_co_u32_e32 v2, vcc, s79, v2
	v_pk_mul_f32 v[76:77], v[76:77], v[6:7]
	s_nop 0
	v_addc_co_u32_e32 v3, vcc, 0, v3, vcc
	v_mov_b64_e32 v[8:9], v[206:207]
	v_mov_b64_e32 v[6:7], v[208:209]
	v_mov_b64_e32 v[4:5], v[210:211]
	s_nop 0
	v_mov_b64_e32 v[2:3], v[212:213]
	s_waitcnt vmcnt(0)
	v_cvt_pk_f32_fp8_e32 v[190:191], v174
	v_cvt_pk_f32_fp8_sdwa v[192:193], v174 src0_sel:WORD_1
	v_cvt_pk_f32_fp8_e32 v[194:195], v175
	v_cvt_pk_f32_fp8_sdwa v[174:175], v175 src0_sel:WORD_1
	v_mul_f32_e32 v11, 0xbfb8aa3b, v190
	v_mul_f32_e32 v190, 0xbfb8aa3b, v191
	v_min_f32_e32 v190, 0x42700000, v190
	v_exp_f32_e32 v196, v190
	v_mul_f32_e32 v190, 0xbfb8aa3b, v192
	v_min_f32_e32 v190, 0x42700000, v190
	v_exp_f32_e32 v197, v190
	v_mul_f32_e32 v190, 0xbfb8aa3b, v193
	v_mul_f32_e32 v174, 0xbfb8aa3b, v174
	v_min_f32_e32 v190, 0x42700000, v190
	v_min_f32_e32 v174, 0x42700000, v174
	v_exp_f32_e32 v198, v190
	v_mul_f32_e32 v190, 0xbfb8aa3b, v194
	v_exp_f32_e32 v201, v174
	v_mul_f32_e32 v174, 0xbfb8aa3b, v175
	v_min_f32_e32 v190, 0x42700000, v190
	v_min_f32_e32 v174, 0x42700000, v174
	v_min_f32_e32 v11, 0x42700000, v11
	v_exp_f32_e32 v199, v190
	v_mul_f32_e32 v190, 0xbfb8aa3b, v195
	v_exp_f32_e32 v202, v174
	v_cvt_pk_f32_fp8_e32 v[174:175], v180
	v_exp_f32_e32 v11, v11
	v_min_f32_e32 v190, 0x42700000, v190
	v_exp_f32_e32 v200, v190
	v_cvt_pk_f32_fp8_sdwa v[190:191], v180 src0_sel:WORD_1
	v_mul_f32_e32 v174, 0xbfb8aa3b, v174
	v_mul_f32_e32 v175, 0xbfb8aa3b, v175
	v_min_f32_e32 v174, 0x42700000, v174
	v_min_f32_e32 v175, 0x42700000, v175
	v_add_f32_e32 v11, 1.0, v11
	v_cvt_pk_f32_fp8_e32 v[192:193], v181
	v_exp_f32_e32 v174, v174
	v_exp_f32_e32 v175, v175
	v_mul_f32_e32 v190, 0xbfb8aa3b, v190
	v_mul_f32_e32 v191, 0xbfb8aa3b, v191
	v_rcp_f32_e32 v194, v11
	v_add_f32_e32 v11, 1.0, v196
	v_min_f32_e32 v190, 0x42700000, v190
	v_min_f32_e32 v191, 0x42700000, v191
	v_rcp_f32_e32 v195, v11
	v_add_f32_e32 v11, 1.0, v197
	v_cvt_pk_f32_fp8_sdwa v[180:181], v181 src0_sel:WORD_1
	v_exp_f32_e32 v190, v190
	v_exp_f32_e32 v191, v191
	v_rcp_f32_e32 v196, v11
	v_add_f32_e32 v11, 1.0, v198
	v_rcp_f32_e32 v197, v11
	v_mul_f32_e32 v192, 0xbfb8aa3b, v192
	v_mul_f32_e32 v193, 0xbfb8aa3b, v193
	v_pk_add_f32 v[174:175], v[174:175], 1.0 op_sel_hi:[1,0]
	v_min_f32_e32 v192, 0x42700000, v192
	v_min_f32_e32 v193, 0x42700000, v193
	v_pk_mul_f32 v[174:175], v[194:195], v[174:175]
	v_add_f32_e32 v11, 1.0, v199
	v_exp_f32_e32 v192, v192
	v_exp_f32_e32 v193, v193
	v_mul_f32_e32 v180, 0xbfb8aa3b, v180
	v_mul_f32_e32 v181, 0xbfb8aa3b, v181
	v_pk_add_f32 v[190:191], v[190:191], 1.0 op_sel_hi:[1,0]
	v_pk_mul_f32 v[72:73], v[72:73], v[174:175]
	v_rcp_f32_e32 v174, v11
	v_add_f32_e32 v11, 1.0, v200
	v_min_f32_e32 v180, 0x42700000, v180
	v_min_f32_e32 v181, 0x42700000, v181
	v_pk_mul_f32 v[190:191], v[196:197], v[190:191]
	v_rcp_f32_e32 v175, v11
	v_add_f32_e32 v11, 1.0, v201
	v_exp_f32_e32 v180, v180
	v_exp_f32_e32 v181, v181
	v_pk_mul_f32 v[74:75], v[74:75], v[190:191]
	v_rcp_f32_e32 v190, v11
	v_add_f32_e32 v11, 1.0, v202
	v_rcp_f32_e32 v191, v11
	v_pk_add_f32 v[192:193], v[192:193], 1.0 op_sel_hi:[1,0]
	v_pk_add_f32 v[180:181], v[180:181], 1.0 op_sel_hi:[1,0]
	v_pk_mul_f32 v[174:175], v[174:175], v[192:193]
	v_pk_mul_f32 v[180:181], v[190:191], v[180:181]
	v_pk_mul_f32 v[68:69], v[68:69], v[174:175]
	v_cvt_pk_f32_fp8_e32 v[174:175], v176
	v_pk_mul_f32 v[70:71], v[70:71], v[180:181]
	v_cvt_pk_f32_fp8_sdwa v[180:181], v176 src0_sel:WORD_1
	v_cvt_pk_f32_fp8_e32 v[190:191], v177
	v_mul_f32_e32 v11, 0xbfb8aa3b, v174
	v_mul_f32_e32 v174, 0xbfb8aa3b, v175
	v_min_f32_e32 v174, 0x42700000, v174
	v_exp_f32_e32 v192, v174
	v_mul_f32_e32 v174, 0xbfb8aa3b, v180
	v_min_f32_e32 v174, 0x42700000, v174
	v_exp_f32_e32 v193, v174
	v_mul_f32_e32 v174, 0xbfb8aa3b, v181
	v_min_f32_e32 v174, 0x42700000, v174
	v_cvt_pk_f32_fp8_sdwa v[176:177], v177 src0_sel:WORD_1
	v_exp_f32_e32 v194, v174
	v_mul_f32_e32 v174, 0xbfb8aa3b, v190
	v_min_f32_e32 v174, 0x42700000, v174
	v_exp_f32_e32 v195, v174
	v_mul_f32_e32 v174, 0xbfb8aa3b, v191
	v_min_f32_e32 v174, 0x42700000, v174
	v_exp_f32_e32 v196, v174
	v_mul_f32_e32 v174, 0xbfb8aa3b, v176
	v_min_f32_e32 v174, 0x42700000, v174
	v_exp_f32_e32 v197, v174
	v_mul_f32_e32 v174, 0xbfb8aa3b, v177
	v_min_f32_e32 v174, 0x42700000, v174
	v_min_f32_e32 v11, 0x42700000, v11
	v_exp_f32_e32 v198, v174
	v_cvt_pk_f32_fp8_e32 v[174:175], v188
	v_exp_f32_e32 v11, v11
	v_cvt_pk_f32_fp8_sdwa v[176:177], v188 src0_sel:WORD_1
	v_cvt_pk_f32_fp8_e32 v[180:181], v189
	v_mul_f32_e32 v174, 0xbfb8aa3b, v174
	v_mul_f32_e32 v175, 0xbfb8aa3b, v175
	v_min_f32_e32 v174, 0x42700000, v174
	v_min_f32_e32 v175, 0x42700000, v175
	v_add_f32_e32 v11, 1.0, v11
	v_exp_f32_e32 v174, v174
	v_exp_f32_e32 v175, v175
	v_mul_f32_e32 v176, 0xbfb8aa3b, v176
	v_mul_f32_e32 v177, 0xbfb8aa3b, v177
	v_rcp_f32_e32 v190, v11
	v_add_f32_e32 v11, 1.0, v192
	v_min_f32_e32 v176, 0x42700000, v176
	v_min_f32_e32 v177, 0x42700000, v177
	v_rcp_f32_e32 v191, v11
	v_add_f32_e32 v11, 1.0, v193
	v_cvt_pk_f32_fp8_sdwa v[188:189], v189 src0_sel:WORD_1
	v_exp_f32_e32 v176, v176
	v_exp_f32_e32 v177, v177
	v_rcp_f32_e32 v192, v11
	v_add_f32_e32 v11, 1.0, v194
	v_rcp_f32_e32 v193, v11
	v_mul_f32_e32 v180, 0xbfb8aa3b, v180
	v_mul_f32_e32 v181, 0xbfb8aa3b, v181
	v_pk_add_f32 v[174:175], v[174:175], 1.0 op_sel_hi:[1,0]
	v_min_f32_e32 v180, 0x42700000, v180
	v_min_f32_e32 v181, 0x42700000, v181
	v_pk_mul_f32 v[174:175], v[190:191], v[174:175]
	v_add_f32_e32 v11, 1.0, v195
	v_exp_f32_e32 v180, v180
	v_exp_f32_e32 v181, v181
	v_mul_f32_e32 v188, 0xbfb8aa3b, v188
	v_mul_f32_e32 v189, 0xbfb8aa3b, v189
	v_pk_add_f32 v[176:177], v[176:177], 1.0 op_sel_hi:[1,0]
	v_pk_mul_f32 v[64:65], v[64:65], v[174:175]
	v_rcp_f32_e32 v174, v11
	v_add_f32_e32 v11, 1.0, v196
	v_min_f32_e32 v188, 0x42700000, v188
	v_min_f32_e32 v189, 0x42700000, v189
	v_pk_mul_f32 v[176:177], v[192:193], v[176:177]
	v_rcp_f32_e32 v175, v11
	v_add_f32_e32 v11, 1.0, v197
	v_exp_f32_e32 v188, v188
	v_exp_f32_e32 v189, v189
	v_pk_mul_f32 v[66:67], v[66:67], v[176:177]
	v_rcp_f32_e32 v176, v11
	v_add_f32_e32 v11, 1.0, v198
	v_rcp_f32_e32 v177, v11
	v_pk_add_f32 v[180:181], v[180:181], 1.0 op_sel_hi:[1,0]
	v_pk_add_f32 v[188:189], v[188:189], 1.0 op_sel_hi:[1,0]
	v_pk_mul_f32 v[174:175], v[174:175], v[180:181]
	v_pk_mul_f32 v[176:177], v[176:177], v[188:189]
	v_pk_mul_f32 v[60:61], v[60:61], v[174:175]
	v_cvt_pk_f32_fp8_e32 v[174:175], v178
	v_pk_mul_f32 v[62:63], v[62:63], v[176:177]
	v_cvt_pk_f32_fp8_sdwa v[176:177], v178 src0_sel:WORD_1
	v_cvt_pk_f32_fp8_e32 v[180:181], v179
	v_mul_f32_e32 v11, 0xbfb8aa3b, v174
	v_mul_f32_e32 v174, 0xbfb8aa3b, v175
	v_min_f32_e32 v174, 0x42700000, v174
	v_exp_f32_e32 v188, v174
	v_mul_f32_e32 v174, 0xbfb8aa3b, v176
	v_min_f32_e32 v174, 0x42700000, v174
	v_exp_f32_e32 v189, v174
	v_mul_f32_e32 v174, 0xbfb8aa3b, v177
	v_min_f32_e32 v174, 0x42700000, v174
	v_cvt_pk_f32_fp8_sdwa v[178:179], v179 src0_sel:WORD_1
	v_exp_f32_e32 v190, v174
	v_mul_f32_e32 v174, 0xbfb8aa3b, v180
	v_min_f32_e32 v174, 0x42700000, v174
	v_exp_f32_e32 v191, v174
	v_mul_f32_e32 v174, 0xbfb8aa3b, v181
	v_min_f32_e32 v174, 0x42700000, v174
	v_exp_f32_e32 v192, v174
	v_mul_f32_e32 v174, 0xbfb8aa3b, v178
	v_min_f32_e32 v174, 0x42700000, v174
	v_exp_f32_e32 v193, v174
	v_mul_f32_e32 v174, 0xbfb8aa3b, v179
	v_min_f32_e32 v174, 0x42700000, v174
	v_min_f32_e32 v11, 0x42700000, v11
	v_exp_f32_e32 v194, v174
	v_cvt_pk_f32_fp8_e32 v[174:175], v172
	v_exp_f32_e32 v11, v11
	v_cvt_pk_f32_fp8_sdwa v[176:177], v172 src0_sel:WORD_1
	v_cvt_pk_f32_fp8_e32 v[178:179], v173
	v_mul_f32_e32 v174, 0xbfb8aa3b, v174
	v_mul_f32_e32 v175, 0xbfb8aa3b, v175
	v_min_f32_e32 v174, 0x42700000, v174
	v_min_f32_e32 v175, 0x42700000, v175
	v_add_f32_e32 v11, 1.0, v11
	v_exp_f32_e32 v174, v174
	v_exp_f32_e32 v175, v175
	v_mul_f32_e32 v176, 0xbfb8aa3b, v176
	v_mul_f32_e32 v177, 0xbfb8aa3b, v177
	v_rcp_f32_e32 v180, v11
	v_add_f32_e32 v11, 1.0, v188
	v_min_f32_e32 v176, 0x42700000, v176
	v_min_f32_e32 v177, 0x42700000, v177
	v_rcp_f32_e32 v181, v11
	v_add_f32_e32 v11, 1.0, v189
	v_cvt_pk_f32_fp8_sdwa v[172:173], v173 src0_sel:WORD_1
	v_exp_f32_e32 v176, v176
	v_exp_f32_e32 v177, v177
	v_rcp_f32_e32 v188, v11
	v_add_f32_e32 v11, 1.0, v190
	v_rcp_f32_e32 v189, v11
	v_pk_add_f32 v[174:175], v[174:175], 1.0 op_sel_hi:[1,0]
	v_add_f32_e32 v11, 1.0, v191
	v_pk_mul_f32 v[174:175], v[180:181], v[174:175]
	v_mul_f32_e32 v172, 0xbfb8aa3b, v172
	v_mul_f32_e32 v173, 0xbfb8aa3b, v173
	v_pk_add_f32 v[176:177], v[176:177], 1.0 op_sel_hi:[1,0]
	v_pk_mul_f32 v[56:57], v[56:57], v[174:175]
	v_rcp_f32_e32 v174, v11
	v_add_f32_e32 v11, 1.0, v192
	v_min_f32_e32 v172, 0x42700000, v172
	v_min_f32_e32 v173, 0x42700000, v173
	v_pk_mul_f32 v[176:177], v[188:189], v[176:177]
	v_rcp_f32_e32 v175, v11
	v_add_f32_e32 v11, 1.0, v193
	v_mul_f32_e32 v178, 0xbfb8aa3b, v178
	v_mul_f32_e32 v179, 0xbfb8aa3b, v179
	v_exp_f32_e32 v172, v172
	v_exp_f32_e32 v173, v173
	v_pk_mul_f32 v[58:59], v[58:59], v[176:177]
	v_rcp_f32_e32 v176, v11
	v_add_f32_e32 v11, 1.0, v194
	v_min_f32_e32 v178, 0x42700000, v178
	v_min_f32_e32 v179, 0x42700000, v179
	v_rcp_f32_e32 v177, v11
	v_exp_f32_e32 v178, v178
	v_exp_f32_e32 v179, v179
	v_pk_add_f32 v[172:173], v[172:173], 1.0 op_sel_hi:[1,0]
	v_pk_add_f32 v[178:179], v[178:179], 1.0 op_sel_hi:[1,0]
	v_pk_mul_f32 v[172:173], v[176:177], v[172:173]
	v_pk_mul_f32 v[174:175], v[174:175], v[178:179]
	v_pk_mul_f32 v[54:55], v[54:55], v[172:173]
	v_cvt_pk_f32_fp8_e32 v[172:173], v170
	v_pk_mul_f32 v[52:53], v[52:53], v[174:175]
	v_cvt_pk_f32_fp8_sdwa v[174:175], v170 src0_sel:WORD_1
	v_cvt_pk_f32_fp8_e32 v[176:177], v171
	v_cvt_pk_f32_fp8_sdwa v[170:171], v171 src0_sel:WORD_1
	v_mul_f32_e32 v11, 0xbfb8aa3b, v172
	v_mul_f32_e32 v172, 0xbfb8aa3b, v173
	v_min_f32_e32 v172, 0x42700000, v172
	v_exp_f32_e32 v178, v172
	v_mul_f32_e32 v172, 0xbfb8aa3b, v174
	v_min_f32_e32 v172, 0x42700000, v172
	v_exp_f32_e32 v179, v172
	v_mul_f32_e32 v172, 0xbfb8aa3b, v175
	v_mul_f32_e32 v170, 0xbfb8aa3b, v170
	v_min_f32_e32 v172, 0x42700000, v172
	v_min_f32_e32 v170, 0x42700000, v170
	v_exp_f32_e32 v180, v172
	v_mul_f32_e32 v172, 0xbfb8aa3b, v176
	v_exp_f32_e32 v189, v170
	v_mul_f32_e32 v170, 0xbfb8aa3b, v171
	v_min_f32_e32 v172, 0x42700000, v172
	v_min_f32_e32 v170, 0x42700000, v170
	v_min_f32_e32 v11, 0x42700000, v11
	v_exp_f32_e32 v181, v172
	v_mul_f32_e32 v172, 0xbfb8aa3b, v177
	v_exp_f32_e32 v190, v170
	v_cvt_pk_f32_fp8_e32 v[170:171], v168
	v_exp_f32_e32 v11, v11
	v_min_f32_e32 v172, 0x42700000, v172
	v_exp_f32_e32 v188, v172
	v_cvt_pk_f32_fp8_sdwa v[172:173], v168 src0_sel:WORD_1
	v_mul_f32_e32 v170, 0xbfb8aa3b, v170
	v_mul_f32_e32 v171, 0xbfb8aa3b, v171
	v_min_f32_e32 v170, 0x42700000, v170
	v_min_f32_e32 v171, 0x42700000, v171
	v_add_f32_e32 v11, 1.0, v11
	v_exp_f32_e32 v170, v170
	v_exp_f32_e32 v171, v171
	v_mul_f32_e32 v172, 0xbfb8aa3b, v172
	v_mul_f32_e32 v173, 0xbfb8aa3b, v173
	v_rcp_f32_e32 v176, v11
	v_add_f32_e32 v11, 1.0, v178
	v_min_f32_e32 v172, 0x42700000, v172
	v_min_f32_e32 v173, 0x42700000, v173
	v_rcp_f32_e32 v177, v11
	v_add_f32_e32 v11, 1.0, v179
	v_cvt_pk_f32_fp8_e32 v[174:175], v169
	v_cvt_pk_f32_fp8_sdwa v[168:169], v169 src0_sel:WORD_1
	v_exp_f32_e32 v172, v172
	v_exp_f32_e32 v173, v173
	v_rcp_f32_e32 v178, v11
	v_add_f32_e32 v11, 1.0, v180
	v_rcp_f32_e32 v179, v11
	v_pk_add_f32 v[170:171], v[170:171], 1.0 op_sel_hi:[1,0]
	v_add_f32_e32 v11, 1.0, v181
	v_pk_mul_f32 v[170:171], v[176:177], v[170:171]
	v_mul_f32_e32 v168, 0xbfb8aa3b, v168
	v_mul_f32_e32 v169, 0xbfb8aa3b, v169
	v_pk_add_f32 v[172:173], v[172:173], 1.0 op_sel_hi:[1,0]
	v_pk_mul_f32 v[48:49], v[48:49], v[170:171]
	v_rcp_f32_e32 v170, v11
	v_add_f32_e32 v11, 1.0, v188
	v_min_f32_e32 v168, 0x42700000, v168
	v_min_f32_e32 v169, 0x42700000, v169
	v_pk_mul_f32 v[172:173], v[178:179], v[172:173]
	v_rcp_f32_e32 v171, v11
	v_add_f32_e32 v11, 1.0, v189
	v_mul_f32_e32 v174, 0xbfb8aa3b, v174
	v_mul_f32_e32 v175, 0xbfb8aa3b, v175
	v_exp_f32_e32 v168, v168
	v_exp_f32_e32 v169, v169
	v_pk_mul_f32 v[50:51], v[50:51], v[172:173]
	v_rcp_f32_e32 v172, v11
	v_add_f32_e32 v11, 1.0, v190
	v_min_f32_e32 v174, 0x42700000, v174
	v_min_f32_e32 v175, 0x42700000, v175
	v_rcp_f32_e32 v173, v11
	v_exp_f32_e32 v174, v174
	v_exp_f32_e32 v175, v175
	v_pk_add_f32 v[168:169], v[168:169], 1.0 op_sel_hi:[1,0]
	v_pk_add_f32 v[174:175], v[174:175], 1.0 op_sel_hi:[1,0]
	v_pk_mul_f32 v[168:169], v[172:173], v[168:169]
	v_pk_mul_f32 v[170:171], v[170:171], v[174:175]
	v_pk_mul_f32 v[46:47], v[46:47], v[168:169]
	v_cvt_pk_f32_fp8_e32 v[168:169], v166
	v_pk_mul_f32 v[44:45], v[44:45], v[170:171]
	v_cvt_pk_f32_fp8_sdwa v[170:171], v166 src0_sel:WORD_1
	v_cvt_pk_f32_fp8_e32 v[172:173], v167
	v_cvt_pk_f32_fp8_sdwa v[166:167], v167 src0_sel:WORD_1
	v_mul_f32_e32 v11, 0xbfb8aa3b, v168
	v_mul_f32_e32 v168, 0xbfb8aa3b, v169
	v_min_f32_e32 v168, 0x42700000, v168
	v_exp_f32_e32 v174, v168
	v_mul_f32_e32 v168, 0xbfb8aa3b, v170
	v_min_f32_e32 v168, 0x42700000, v168
	v_exp_f32_e32 v175, v168
	v_mul_f32_e32 v168, 0xbfb8aa3b, v171
	v_mul_f32_e32 v166, 0xbfb8aa3b, v166
	v_min_f32_e32 v168, 0x42700000, v168
	v_min_f32_e32 v166, 0x42700000, v166
	v_exp_f32_e32 v176, v168
	v_mul_f32_e32 v168, 0xbfb8aa3b, v172
	v_exp_f32_e32 v179, v166
	v_mul_f32_e32 v166, 0xbfb8aa3b, v167
	v_min_f32_e32 v168, 0x42700000, v168
	v_min_f32_e32 v166, 0x42700000, v166
	v_min_f32_e32 v11, 0x42700000, v11
	v_exp_f32_e32 v177, v168
	v_mul_f32_e32 v168, 0xbfb8aa3b, v173
	v_exp_f32_e32 v180, v166
	v_cvt_pk_f32_fp8_e32 v[166:167], v164
	v_exp_f32_e32 v11, v11
	v_min_f32_e32 v168, 0x42700000, v168
	v_exp_f32_e32 v178, v168
	v_cvt_pk_f32_fp8_sdwa v[168:169], v164 src0_sel:WORD_1
	v_mul_f32_e32 v166, 0xbfb8aa3b, v166
	v_mul_f32_e32 v167, 0xbfb8aa3b, v167
	v_min_f32_e32 v166, 0x42700000, v166
	v_min_f32_e32 v167, 0x42700000, v167
	v_add_f32_e32 v11, 1.0, v11
	v_exp_f32_e32 v166, v166
	v_exp_f32_e32 v167, v167
	v_mul_f32_e32 v168, 0xbfb8aa3b, v168
	v_mul_f32_e32 v169, 0xbfb8aa3b, v169
	v_rcp_f32_e32 v172, v11
	v_add_f32_e32 v11, 1.0, v174
	v_min_f32_e32 v168, 0x42700000, v168
	v_min_f32_e32 v169, 0x42700000, v169
	v_rcp_f32_e32 v173, v11
	v_add_f32_e32 v11, 1.0, v175
	v_cvt_pk_f32_fp8_e32 v[170:171], v165
	v_cvt_pk_f32_fp8_sdwa v[164:165], v165 src0_sel:WORD_1
	v_exp_f32_e32 v168, v168
	v_exp_f32_e32 v169, v169
	v_rcp_f32_e32 v174, v11
	v_add_f32_e32 v11, 1.0, v176
	v_rcp_f32_e32 v175, v11
	v_pk_add_f32 v[166:167], v[166:167], 1.0 op_sel_hi:[1,0]
	v_add_f32_e32 v11, 1.0, v177
	v_pk_mul_f32 v[166:167], v[172:173], v[166:167]
	v_mul_f32_e32 v164, 0xbfb8aa3b, v164
	v_mul_f32_e32 v165, 0xbfb8aa3b, v165
	v_pk_add_f32 v[168:169], v[168:169], 1.0 op_sel_hi:[1,0]
	v_pk_mul_f32 v[40:41], v[40:41], v[166:167]
	v_rcp_f32_e32 v166, v11
	v_add_f32_e32 v11, 1.0, v178
	v_min_f32_e32 v164, 0x42700000, v164
	v_min_f32_e32 v165, 0x42700000, v165
	v_pk_mul_f32 v[168:169], v[174:175], v[168:169]
	v_rcp_f32_e32 v167, v11
	v_add_f32_e32 v11, 1.0, v179
	v_mul_f32_e32 v170, 0xbfb8aa3b, v170
	v_mul_f32_e32 v171, 0xbfb8aa3b, v171
	v_exp_f32_e32 v164, v164
	v_exp_f32_e32 v165, v165
	v_pk_mul_f32 v[42:43], v[42:43], v[168:169]
	v_rcp_f32_e32 v168, v11
	v_add_f32_e32 v11, 1.0, v180
	v_min_f32_e32 v170, 0x42700000, v170
	v_min_f32_e32 v171, 0x42700000, v171
	v_rcp_f32_e32 v169, v11
	v_exp_f32_e32 v170, v170
	v_exp_f32_e32 v171, v171
	v_pk_add_f32 v[164:165], v[164:165], 1.0 op_sel_hi:[1,0]
	v_pk_add_f32 v[170:171], v[170:171], 1.0 op_sel_hi:[1,0]
	v_pk_mul_f32 v[164:165], v[168:169], v[164:165]
	v_pk_mul_f32 v[166:167], v[166:167], v[170:171]
	v_pk_mul_f32 v[38:39], v[38:39], v[164:165]
	v_cvt_pk_f32_fp8_e32 v[164:165], v162
	v_pk_mul_f32 v[36:37], v[36:37], v[166:167]
	v_cvt_pk_f32_fp8_sdwa v[166:167], v162 src0_sel:WORD_1
	v_cvt_pk_f32_fp8_e32 v[168:169], v163
	v_cvt_pk_f32_fp8_sdwa v[162:163], v163 src0_sel:WORD_1
	v_mul_f32_e32 v11, 0xbfb8aa3b, v164
	v_mul_f32_e32 v164, 0xbfb8aa3b, v165
	v_min_f32_e32 v164, 0x42700000, v164
	v_exp_f32_e32 v170, v164
	v_mul_f32_e32 v164, 0xbfb8aa3b, v166
	v_min_f32_e32 v164, 0x42700000, v164
	v_exp_f32_e32 v171, v164
	v_mul_f32_e32 v164, 0xbfb8aa3b, v167
	v_mul_f32_e32 v162, 0xbfb8aa3b, v162
	v_min_f32_e32 v164, 0x42700000, v164
	v_min_f32_e32 v162, 0x42700000, v162
	v_exp_f32_e32 v172, v164
	v_mul_f32_e32 v164, 0xbfb8aa3b, v168
	v_exp_f32_e32 v175, v162
	v_mul_f32_e32 v162, 0xbfb8aa3b, v163
	v_min_f32_e32 v164, 0x42700000, v164
	v_min_f32_e32 v162, 0x42700000, v162
	v_min_f32_e32 v11, 0x42700000, v11
	v_exp_f32_e32 v173, v164
	v_mul_f32_e32 v164, 0xbfb8aa3b, v169
	v_exp_f32_e32 v176, v162
	v_cvt_pk_f32_fp8_e32 v[162:163], v160
	v_exp_f32_e32 v11, v11
	v_min_f32_e32 v164, 0x42700000, v164
	v_exp_f32_e32 v174, v164
	v_cvt_pk_f32_fp8_sdwa v[164:165], v160 src0_sel:WORD_1
	v_mul_f32_e32 v162, 0xbfb8aa3b, v162
	v_mul_f32_e32 v163, 0xbfb8aa3b, v163
	v_min_f32_e32 v162, 0x42700000, v162
	v_min_f32_e32 v163, 0x42700000, v163
	v_add_f32_e32 v11, 1.0, v11
	v_exp_f32_e32 v162, v162
	v_exp_f32_e32 v163, v163
	v_mul_f32_e32 v164, 0xbfb8aa3b, v164
	v_mul_f32_e32 v165, 0xbfb8aa3b, v165
	v_rcp_f32_e32 v168, v11
	v_add_f32_e32 v11, 1.0, v170
	v_min_f32_e32 v164, 0x42700000, v164
	v_min_f32_e32 v165, 0x42700000, v165
	v_rcp_f32_e32 v169, v11
	v_add_f32_e32 v11, 1.0, v171
	v_cvt_pk_f32_fp8_e32 v[166:167], v161
	v_cvt_pk_f32_fp8_sdwa v[160:161], v161 src0_sel:WORD_1
	v_exp_f32_e32 v164, v164
	v_exp_f32_e32 v165, v165
	v_rcp_f32_e32 v170, v11
	v_add_f32_e32 v11, 1.0, v172
	v_rcp_f32_e32 v171, v11
	v_pk_add_f32 v[162:163], v[162:163], 1.0 op_sel_hi:[1,0]
	v_add_f32_e32 v11, 1.0, v173
	v_pk_mul_f32 v[162:163], v[168:169], v[162:163]
	v_mul_f32_e32 v160, 0xbfb8aa3b, v160
	v_mul_f32_e32 v161, 0xbfb8aa3b, v161
	v_pk_add_f32 v[164:165], v[164:165], 1.0 op_sel_hi:[1,0]
	v_pk_mul_f32 v[32:33], v[32:33], v[162:163]
	v_rcp_f32_e32 v162, v11
	v_add_f32_e32 v11, 1.0, v174
	v_min_f32_e32 v160, 0x42700000, v160
	v_min_f32_e32 v161, 0x42700000, v161
	v_pk_mul_f32 v[164:165], v[170:171], v[164:165]
	v_rcp_f32_e32 v163, v11
	v_add_f32_e32 v11, 1.0, v175
	v_mul_f32_e32 v166, 0xbfb8aa3b, v166
	v_mul_f32_e32 v167, 0xbfb8aa3b, v167
	v_exp_f32_e32 v160, v160
	v_exp_f32_e32 v161, v161
	v_pk_mul_f32 v[34:35], v[34:35], v[164:165]
	v_rcp_f32_e32 v164, v11
	v_add_f32_e32 v11, 1.0, v176
	v_min_f32_e32 v166, 0x42700000, v166
	v_min_f32_e32 v167, 0x42700000, v167
	v_rcp_f32_e32 v165, v11
	v_exp_f32_e32 v166, v166
	v_exp_f32_e32 v167, v167
	v_pk_add_f32 v[160:161], v[160:161], 1.0 op_sel_hi:[1,0]
	v_pk_add_f32 v[166:167], v[166:167], 1.0 op_sel_hi:[1,0]
	v_pk_mul_f32 v[160:161], v[164:165], v[160:161]
	v_pk_mul_f32 v[162:163], v[162:163], v[166:167]
	v_pk_mul_f32 v[30:31], v[30:31], v[160:161]
	v_cvt_pk_f32_fp8_e32 v[160:161], v8
	v_pk_mul_f32 v[28:29], v[28:29], v[162:163]
	v_cvt_pk_f32_fp8_sdwa v[162:163], v8 src0_sel:WORD_1
	v_cvt_pk_f32_fp8_e32 v[164:165], v9
	v_mul_f32_e32 v11, 0xbfb8aa3b, v160
	v_mul_f32_e32 v160, 0xbfb8aa3b, v161
	v_min_f32_e32 v160, 0x42700000, v160
	v_exp_f32_e32 v166, v160
	v_mul_f32_e32 v160, 0xbfb8aa3b, v162
	v_min_f32_e32 v160, 0x42700000, v160
	v_exp_f32_e32 v167, v160
	v_mul_f32_e32 v160, 0xbfb8aa3b, v163
	v_min_f32_e32 v160, 0x42700000, v160
	v_cvt_pk_f32_fp8_sdwa v[8:9], v9 src0_sel:WORD_1
	v_exp_f32_e32 v168, v160
	v_mul_f32_e32 v160, 0xbfb8aa3b, v164
	v_min_f32_e32 v160, 0x42700000, v160
	v_min_f32_e32 v11, 0x42700000, v11
	v_exp_f32_e32 v169, v160
	v_mul_f32_e32 v160, 0xbfb8aa3b, v165
	v_exp_f32_e32 v11, v11
	v_min_f32_e32 v160, 0x42700000, v160
	v_exp_f32_e32 v170, v160
	v_mul_f32_e32 v8, 0xbfb8aa3b, v8
	v_cvt_pk_f32_fp8_sdwa v[160:161], v6 src0_sel:WORD_1
	v_min_f32_e32 v8, 0x42700000, v8
	v_exp_f32_e32 v171, v8
	v_mul_f32_e32 v8, 0xbfb8aa3b, v9
	v_min_f32_e32 v8, 0x42700000, v8
	v_add_f32_e32 v11, 1.0, v11
	v_exp_f32_e32 v172, v8
	v_cvt_pk_f32_fp8_e32 v[8:9], v6
	v_mul_f32_e32 v160, 0xbfb8aa3b, v160
	v_mul_f32_e32 v161, 0xbfb8aa3b, v161
	v_rcp_f32_e32 v164, v11
	v_add_f32_e32 v11, 1.0, v166
	v_min_f32_e32 v160, 0x42700000, v160
	v_min_f32_e32 v161, 0x42700000, v161
	v_rcp_f32_e32 v165, v11
	v_add_f32_e32 v11, 1.0, v167
	v_cvt_pk_f32_fp8_e32 v[162:163], v7
	v_cvt_pk_f32_fp8_sdwa v[6:7], v7 src0_sel:WORD_1
	v_exp_f32_e32 v160, v160
	v_exp_f32_e32 v161, v161
	v_rcp_f32_e32 v166, v11
	v_add_f32_e32 v11, 1.0, v168
	v_rcp_f32_e32 v167, v11
	v_mul_f32_e32 v8, 0xbfb8aa3b, v8
	v_mul_f32_e32 v9, 0xbfb8aa3b, v9
	v_min_f32_e32 v8, 0x42700000, v8
	v_min_f32_e32 v9, 0x42700000, v9
	v_exp_f32_e32 v8, v8
	v_exp_f32_e32 v9, v9
	v_mul_f32_e32 v6, 0xbfb8aa3b, v6
	v_mul_f32_e32 v7, 0xbfb8aa3b, v7
	v_pk_add_f32 v[160:161], v[160:161], 1.0 op_sel_hi:[1,0]
	v_min_f32_e32 v6, 0x42700000, v6
	v_min_f32_e32 v7, 0x42700000, v7
	v_pk_mul_f32 v[160:161], v[166:167], v[160:161]
	v_add_f32_e32 v11, 1.0, v171
	v_exp_f32_e32 v6, v6
	v_exp_f32_e32 v7, v7
	v_pk_mul_f32 v[26:27], v[26:27], v[160:161]
	v_rcp_f32_e32 v160, v11
	v_add_f32_e32 v11, 1.0, v172
	v_rcp_f32_e32 v161, v11
	v_mul_f32_e32 v162, 0xbfb8aa3b, v162
	v_mul_f32_e32 v163, 0xbfb8aa3b, v163
	v_pk_add_f32 v[8:9], v[8:9], 1.0 op_sel_hi:[1,0]
	v_min_f32_e32 v162, 0x42700000, v162
	v_min_f32_e32 v163, 0x42700000, v163
	v_pk_mul_f32 v[8:9], v[164:165], v[8:9]
	v_exp_f32_e32 v162, v162
	v_exp_f32_e32 v163, v163
	v_pk_mul_f32 v[24:25], v[24:25], v[8:9]
	v_add_f32_e32 v8, 1.0, v169
	v_add_f32_e32 v9, 1.0, v170
	v_pk_add_f32 v[6:7], v[6:7], 1.0 op_sel_hi:[1,0]
	v_rcp_f32_e32 v8, v8
	v_rcp_f32_e32 v9, v9
	v_pk_mul_f32 v[6:7], v[160:161], v[6:7]
	v_pk_add_f32 v[162:163], v[162:163], 1.0 op_sel_hi:[1,0]
	v_pk_mul_f32 v[22:23], v[22:23], v[6:7]
	v_cvt_pk_f32_fp8_e32 v[6:7], v4
	v_pk_mul_f32 v[8:9], v[8:9], v[162:163]
	v_cvt_pk_f32_fp8_e32 v[160:161], v5
	v_pk_mul_f32 v[20:21], v[20:21], v[8:9]
	v_cvt_pk_f32_fp8_sdwa v[8:9], v4 src0_sel:WORD_1
	v_mul_f32_e32 v6, 0xbfb8aa3b, v6
	v_min_f32_e32 v6, 0x42700000, v6
	v_exp_f32_e32 v11, v6
	v_mul_f32_e32 v6, 0xbfb8aa3b, v7
	v_min_f32_e32 v6, 0x42700000, v6
	v_cvt_pk_f32_fp8_sdwa v[4:5], v5 src0_sel:WORD_1
	v_exp_f32_e32 v162, v6
	v_mul_f32_e32 v6, 0xbfb8aa3b, v8
	v_min_f32_e32 v6, 0x42700000, v6
	v_exp_f32_e32 v163, v6
	v_mul_f32_e32 v6, 0xbfb8aa3b, v9
	v_min_f32_e32 v6, 0x42700000, v6
	v_exp_f32_e32 v164, v6
	v_mul_f32_e32 v6, 0xbfb8aa3b, v160
	v_mul_f32_e32 v4, 0xbfb8aa3b, v4
	v_min_f32_e32 v6, 0x42700000, v6
	v_min_f32_e32 v4, 0x42700000, v4
	v_exp_f32_e32 v165, v6
	v_mul_f32_e32 v6, 0xbfb8aa3b, v161
	v_exp_f32_e32 v167, v4
	v_mul_f32_e32 v4, 0xbfb8aa3b, v5
	v_min_f32_e32 v6, 0x42700000, v6
	v_min_f32_e32 v4, 0x42700000, v4
	v_exp_f32_e32 v166, v6
	v_exp_f32_e32 v168, v4
	v_cvt_pk_f32_fp8_e32 v[4:5], v2
	v_cvt_pk_f32_fp8_sdwa v[6:7], v2 src0_sel:WORD_1
	v_add_f32_e32 v11, 1.0, v11
	v_rcp_f32_e32 v160, v11
	v_mul_f32_e32 v4, 0xbfb8aa3b, v4
	v_mul_f32_e32 v5, 0xbfb8aa3b, v5
	v_mul_f32_e32 v6, 0xbfb8aa3b, v6
	v_mul_f32_e32 v7, 0xbfb8aa3b, v7
	v_add_f32_e32 v11, 1.0, v162
	v_min_f32_e32 v4, 0x42700000, v4
	v_min_f32_e32 v5, 0x42700000, v5
	v_min_f32_e32 v6, 0x42700000, v6
	v_min_f32_e32 v7, 0x42700000, v7
	v_rcp_f32_e32 v161, v11
	v_add_f32_e32 v11, 1.0, v163
	v_cvt_pk_f32_fp8_e32 v[8:9], v3
	v_cvt_pk_f32_fp8_sdwa v[2:3], v3 src0_sel:WORD_1
	v_exp_f32_e32 v4, v4
	v_exp_f32_e32 v5, v5
	v_exp_f32_e32 v6, v6
	v_exp_f32_e32 v7, v7
	v_rcp_f32_e32 v162, v11
	v_add_f32_e32 v11, 1.0, v164
	v_rcp_f32_e32 v163, v11
	v_mul_f32_e32 v8, 0xbfb8aa3b, v8
	v_mul_f32_e32 v9, 0xbfb8aa3b, v9
	v_mul_f32_e32 v2, 0xbfb8aa3b, v2
	v_mul_f32_e32 v3, 0xbfb8aa3b, v3
	v_pk_add_f32 v[6:7], v[6:7], 1.0 op_sel_hi:[1,0]
	v_pk_add_f32 v[4:5], v[4:5], 1.0 op_sel_hi:[1,0]
	v_min_f32_e32 v8, 0x42700000, v8
	v_min_f32_e32 v9, 0x42700000, v9
	v_min_f32_e32 v2, 0x42700000, v2
	v_min_f32_e32 v3, 0x42700000, v3
	v_pk_mul_f32 v[4:5], v[160:161], v[4:5]
	v_pk_mul_f32 v[6:7], v[162:163], v[6:7]
	v_exp_f32_e32 v8, v8
	v_exp_f32_e32 v9, v9
	v_exp_f32_e32 v2, v2
	v_exp_f32_e32 v3, v3
	v_pk_mul_f32 v[18:19], v[18:19], v[6:7]
	v_pk_mul_f32 v[16:17], v[16:17], v[4:5]
	v_add_f32_e32 v4, 1.0, v165
	v_add_f32_e32 v5, 1.0, v166
	v_add_f32_e32 v6, 1.0, v167
	v_add_f32_e32 v7, 1.0, v168
	v_rcp_f32_e32 v4, v4
	v_rcp_f32_e32 v5, v5
	v_rcp_f32_e32 v6, v6
	v_rcp_f32_e32 v7, v7
	v_pk_add_f32 v[2:3], v[2:3], 1.0 op_sel_hi:[1,0]
	v_pk_add_f32 v[8:9], v[8:9], 1.0 op_sel_hi:[1,0]
	v_pk_mul_f32 v[2:3], v[6:7], v[2:3]
	v_pk_mul_f32 v[4:5], v[4:5], v[8:9]
	v_pk_mul_f32 v[14:15], v[14:15], v[2:3]
	v_pk_mul_f32 v[12:13], v[12:13], v[4:5]
	s_nop 0
	s_branch .LBB0_890

.LBB0_895:
	v_add_u32_e32 v166, s83, v182
	v_ashrrev_i32_e32 v167, 31, v166
	v_add_u32_e32 v2, s84, v184
	v_lshlrev_b64 v[4:5], 11, v[166:167]
	s_nop 15
	s_nop 15
	v_lshl_add_u64 v[4:5], s[92:93], 0, v[4:5]
	v_ashrrev_i32_e32 v3, 31, v2
	v_lshl_add_u64 v[4:5], v[4:5], 0, v[2:3]
	global_load_dwordx2 v[168:169], v[4:5], off offset:1024 nt
	global_load_dwordx2 v[164:165], v[4:5], off offset:1152 nt
	v_add_co_u32_e32 v6, vcc, s74, v4
	v_lshlrev_b64 v[166:167], 10, v[166:167]
	s_nop 0
	v_addc_co_u32_e32 v7, vcc, 0, v5, vcc
	global_load_dwordx2 v[162:163], v[6:7], off offset:1024 nt
	global_load_dwordx2 v[160:161], v[6:7], off offset:1152 nt
	v_add_co_u32_e32 v6, vcc, s61, v4
	s_mov_b64 s[0:1], 0x4000
	s_nop 0
	v_addc_co_u32_e32 v7, vcc, 0, v5, vcc
	global_load_dwordx2 v[158:159], v[6:7], off offset:1024 nt
	global_load_dwordx2 v[156:157], v[6:7], off offset:1152 nt
	v_add_co_u32_e32 v208, vcc, s73, v4
	s_nop 1
	v_addc_co_u32_e32 v209, vcc, 0, v5, vcc
	global_load_dwordx2 v[188:189], v[208:209], off offset:1024 nt
	global_load_dwordx2 v[190:191], v[208:209], off offset:1152 nt
	v_add_co_u32_e32 v208, vcc, s76, v4
	s_nop 1
	v_addc_co_u32_e32 v209, vcc, 0, v5, vcc
	global_load_dwordx2 v[192:193], v[208:209], off offset:1024 nt
	global_load_dwordx2 v[194:195], v[208:209], off offset:1152 nt
	v_add_co_u32_e32 v208, vcc, s77, v4
	s_nop 1
	v_addc_co_u32_e32 v209, vcc, 0, v5, vcc
	global_load_dwordx2 v[196:197], v[208:209], off offset:1024 nt
	global_load_dwordx2 v[198:199], v[208:209], off offset:1152 nt
	v_add_co_u32_e32 v208, vcc, s78, v4
	s_nop 1
	v_addc_co_u32_e32 v209, vcc, 0, v5, vcc
	global_load_dwordx2 v[200:201], v[208:209], off offset:1024 nt
	global_load_dwordx2 v[202:203], v[208:209], off offset:1152 nt
	v_add_co_u32_e32 v208, vcc, s79, v4
	s_nop 1
	v_addc_co_u32_e32 v209, vcc, 0, v5, vcc
	global_load_dwordx2 v[204:205], v[208:209], off offset:1024 nt
	global_load_dwordx2 v[206:207], v[208:209], off offset:1152 nt
	v_add_co_u32_e32 v6, vcc, s73, v4
	s_waitcnt vmcnt(0)
	v_cvt_pk_f32_fp8_e32 v[170:171], v168
	v_cvt_pk_f32_fp8_sdwa v[172:173], v168 src0_sel:WORD_1
	v_cvt_pk_f32_fp8_e32 v[174:175], v169
	v_cvt_pk_f32_fp8_sdwa v[168:169], v169 src0_sel:WORD_1
	v_mul_f32_e32 v11, 0xbfb8aa3b, v170
	v_min_f32_e32 v11, 0x42700000, v11
	v_exp_f32_e32 v11, v11
	v_mul_f32_e32 v170, 0xbfb8aa3b, v171
	v_min_f32_e32 v170, 0x42700000, v170
	v_exp_f32_e32 v170, v170
	v_add_f32_e32 v11, 1.0, v11
	v_rcp_f32_e32 v11, v11
	v_mul_f32_e32 v171, 0xbfb8aa3b, v172
	v_min_f32_e32 v171, 0x42700000, v171
	v_exp_f32_e32 v171, v171
	v_mul_f32_e32 v11, v136, v11
	v_add_f32_e32 v136, 1.0, v170
	v_rcp_f32_e32 v136, v136
	v_mul_f32_e32 v172, 0xbfb8aa3b, v173
	v_min_f32_e32 v172, 0x42700000, v172
	v_exp_f32_e32 v172, v172
	v_mul_f32_e32 v136, v137, v136
	v_add_f32_e32 v137, 1.0, v171
	v_rcp_f32_e32 v137, v137
	v_mul_f32_e32 v173, 0xbfb8aa3b, v174
	v_min_f32_e32 v173, 0x42700000, v173
	v_exp_f32_e32 v173, v173
	v_mul_f32_e32 v137, v138, v137
	v_add_f32_e32 v138, 1.0, v172
	v_rcp_f32_e32 v138, v138
	v_mul_f32_e32 v174, 0xbfb8aa3b, v175
	v_min_f32_e32 v174, 0x42700000, v174
	v_exp_f32_e32 v174, v174
	v_mul_f32_e32 v138, v139, v138
	v_add_f32_e32 v139, 1.0, v173
	v_rcp_f32_e32 v139, v139
	v_mul_f32_e32 v168, 0xbfb8aa3b, v168
	v_min_f32_e32 v168, 0x42700000, v168
	v_exp_f32_e32 v168, v168
	v_mul_f32_e32 v139, v132, v139
	v_add_f32_e32 v132, 1.0, v174
	v_rcp_f32_e32 v132, v132
	v_mul_f32_e32 v169, 0xbfb8aa3b, v169
	v_min_f32_e32 v169, 0x42700000, v169
	v_exp_f32_e32 v169, v169
	v_mul_f32_e32 v170, v133, v132
	v_add_f32_e32 v132, 1.0, v168
	v_rcp_f32_e32 v132, v132
	v_mov_b32_e32 v133, 0
	v_cvt_pk_fp8_f32 v133, v139, v170
	v_addc_co_u32_e32 v7, vcc, 0, v5, vcc
	v_mul_f32_e32 v134, v134, v132
	v_add_f32_e32 v132, 1.0, v169
	v_rcp_f32_e32 v132, v132
	v_mov_b64_e32 v[8:9], v[188:189]
	s_nop 0
	v_mov_b64_e32 v[6:7], v[190:191]
	v_mul_f32_e32 v135, v135, v132
	v_mov_b32_e32 v132, 0
	v_cvt_pk_fp8_f32 v132, v11, v136
	v_cvt_pk_fp8_f32 v133, v134, v135 op_sel:[0,0,1]
	v_lshl_add_u64 v[134:135], s[24:25], 0, v[166:167]
	v_lshl_add_u64 v[2:3], v[134:135], 0, v[2:3]
	v_cvt_pk_fp8_f32 v132, v137, v138 op_sel:[0,0,1]
	v_cvt_pk_f32_fp8_e32 v[136:137], v164
	v_cvt_pk_f32_fp8_sdwa v[138:139], v164 src0_sel:WORD_1
	v_cvt_pk_f32_fp8_e32 v[134:135], v165
	global_store_dwordx2 v[2:3], v[132:133], off
	v_mul_f32_e32 v11, 0xbfb8aa3b, v136
	v_min_f32_e32 v11, 0x42700000, v11
	v_exp_f32_e32 v11, v11
	v_mul_f32_e32 v136, 0xbfb8aa3b, v137
	v_min_f32_e32 v136, 0x42700000, v136
	v_exp_f32_e32 v136, v136
	v_add_f32_e32 v11, 1.0, v11
	v_rcp_f32_e32 v11, v11
	v_mul_f32_e32 v137, 0xbfb8aa3b, v138
	v_min_f32_e32 v137, 0x42700000, v137
	v_exp_f32_e32 v137, v137
	v_mul_f32_e32 v11, v128, v11
	v_add_f32_e32 v128, 1.0, v136
	v_rcp_f32_e32 v128, v128
	v_mul_f32_e32 v138, 0xbfb8aa3b, v139
	v_min_f32_e32 v138, 0x42700000, v138
	v_exp_f32_e32 v138, v138
	v_mul_f32_e32 v128, v129, v128
	v_add_f32_e32 v129, 1.0, v137
	v_rcp_f32_e32 v129, v129
	v_mul_f32_e32 v134, 0xbfb8aa3b, v134
	v_min_f32_e32 v134, 0x42700000, v134
	v_exp_f32_e32 v134, v134
	v_mul_f32_e32 v129, v130, v129
	v_add_f32_e32 v130, 1.0, v138
	v_rcp_f32_e32 v130, v130
	v_mul_f32_e32 v135, 0xbfb8aa3b, v135
	v_cvt_pk_f32_fp8_sdwa v[132:133], v165 src0_sel:WORD_1
	v_min_f32_e32 v135, 0x42700000, v135
	v_mul_f32_e32 v130, v131, v130
	v_add_f32_e32 v131, 1.0, v134
	v_exp_f32_e32 v135, v135
	v_rcp_f32_e32 v131, v131
	v_mul_f32_e32 v132, 0xbfb8aa3b, v132
	v_min_f32_e32 v132, 0x42700000, v132
	v_exp_f32_e32 v132, v132
	v_mul_f32_e32 v131, v124, v131
	v_add_f32_e32 v124, 1.0, v135
	v_rcp_f32_e32 v124, v124
	v_mul_f32_e32 v133, 0xbfb8aa3b, v133
	v_min_f32_e32 v133, 0x42700000, v133
	v_exp_f32_e32 v133, v133
	v_mul_f32_e32 v134, v125, v124
	v_add_f32_e32 v124, 1.0, v132
	v_rcp_f32_e32 v124, v124
	v_mov_b32_e32 v125, 0
	v_cvt_pk_fp8_f32 v125, v131, v134
	v_mul_f32_e32 v126, v126, v124
	v_add_f32_e32 v124, 1.0, v133
	v_rcp_f32_e32 v124, v124
	s_nop 0
	v_mul_f32_e32 v127, v127, v124
	v_mov_b32_e32 v124, 0
	v_cvt_pk_fp8_f32 v124, v11, v128
	v_cvt_pk_fp8_f32 v125, v126, v127 op_sel:[0,0,1]
	v_cvt_pk_f32_fp8_sdwa v[126:127], v162 src0_sel:WORD_1
	v_cvt_pk_fp8_f32 v124, v129, v130 op_sel:[0,0,1]
	v_cvt_pk_f32_fp8_e32 v[128:129], v163
	v_cvt_pk_f32_fp8_sdwa v[130:131], v163 src0_sel:WORD_1
	global_store_dwordx2 v[2:3], v[124:125], off offset:128
	v_cvt_pk_f32_fp8_e32 v[124:125], v162
	v_mul_f32_e32 v11, 0xbfb8aa3b, v124
	v_min_f32_e32 v11, 0x42700000, v11
	v_exp_f32_e32 v11, v11
	v_mul_f32_e32 v124, 0xbfb8aa3b, v125
	v_min_f32_e32 v124, 0x42700000, v124
	v_exp_f32_e32 v124, v124
	v_add_f32_e32 v11, 1.0, v11
	v_rcp_f32_e32 v11, v11
	v_mul_f32_e32 v125, 0xbfb8aa3b, v126
	v_min_f32_e32 v125, 0x42700000, v125
	v_exp_f32_e32 v125, v125
	v_mul_f32_e32 v11, v120, v11
	v_add_f32_e32 v120, 1.0, v124
	v_rcp_f32_e32 v120, v120
	v_mul_f32_e32 v126, 0xbfb8aa3b, v127
	v_min_f32_e32 v126, 0x42700000, v126
	v_exp_f32_e32 v126, v126
	v_mul_f32_e32 v120, v121, v120
	v_add_f32_e32 v121, 1.0, v125
	v_rcp_f32_e32 v121, v121
	v_mul_f32_e32 v127, 0xbfb8aa3b, v128
	v_min_f32_e32 v127, 0x42700000, v127
	v_exp_f32_e32 v127, v127
	v_mul_f32_e32 v121, v122, v121
	v_add_f32_e32 v122, 1.0, v126
	v_rcp_f32_e32 v122, v122
	v_mul_f32_e32 v128, 0xbfb8aa3b, v129
	v_min_f32_e32 v128, 0x42700000, v128
	v_exp_f32_e32 v128, v128
	v_mul_f32_e32 v122, v123, v122
	v_add_f32_e32 v123, 1.0, v127
	v_rcp_f32_e32 v123, v123
	v_mul_f32_e32 v129, 0xbfb8aa3b, v130
	v_min_f32_e32 v129, 0x42700000, v129
	v_exp_f32_e32 v129, v129
	v_mul_f32_e32 v123, v116, v123
	v_add_f32_e32 v116, 1.0, v128
	v_rcp_f32_e32 v116, v116
	v_mul_f32_e32 v130, 0xbfb8aa3b, v131
	v_min_f32_e32 v130, 0x42700000, v130
	v_exp_f32_e32 v130, v130
	v_mul_f32_e32 v124, v117, v116
	v_add_f32_e32 v116, 1.0, v129
	v_rcp_f32_e32 v116, v116
	v_mov_b32_e32 v117, 0
	v_cvt_pk_fp8_f32 v117, v123, v124
	v_cvt_pk_f32_fp8_sdwa v[124:125], v161 src0_sel:WORD_1
	v_mul_f32_e32 v118, v118, v116
	v_add_f32_e32 v116, 1.0, v130
	v_rcp_f32_e32 v116, v116
	s_nop 0
	v_mul_f32_e32 v119, v119, v116
	v_mov_b32_e32 v116, 0
	v_cvt_pk_fp8_f32 v116, v11, v120
	v_cvt_pk_fp8_f32 v117, v118, v119 op_sel:[0,0,1]
	v_lshl_add_u64 v[118:119], v[2:3], 0, s[0:1]
	s_movk_i32 s0, 0x4000
	v_cvt_pk_fp8_f32 v116, v121, v122 op_sel:[0,0,1]
	v_add_co_u32_e32 v120, vcc, s0, v2
	v_cvt_pk_f32_fp8_e32 v[122:123], v161
	s_nop 0
	v_addc_co_u32_e32 v121, vcc, 0, v3, vcc
	global_store_dwordx2 v[120:121], v[116:117], off
	v_cvt_pk_f32_fp8_e32 v[116:117], v160
	v_cvt_pk_f32_fp8_sdwa v[120:121], v160 src0_sel:WORD_1
	s_mov_b64 s[0:1], 0x8000
	v_mul_f32_e32 v11, 0xbfb8aa3b, v116
	v_min_f32_e32 v11, 0x42700000, v11
	v_exp_f32_e32 v11, v11
	v_mul_f32_e32 v116, 0xbfb8aa3b, v117
	v_min_f32_e32 v116, 0x42700000, v116
	v_exp_f32_e32 v116, v116
	v_add_f32_e32 v11, 1.0, v11
	v_rcp_f32_e32 v11, v11
	v_mul_f32_e32 v117, 0xbfb8aa3b, v120
	v_min_f32_e32 v117, 0x42700000, v117
	v_exp_f32_e32 v117, v117
	v_mul_f32_e32 v11, v112, v11
	v_add_f32_e32 v112, 1.0, v116
	v_rcp_f32_e32 v112, v112
	v_mul_f32_e32 v120, 0xbfb8aa3b, v121
	v_min_f32_e32 v120, 0x42700000, v120
	v_exp_f32_e32 v120, v120
	v_mul_f32_e32 v112, v113, v112
	v_add_f32_e32 v113, 1.0, v117
	v_rcp_f32_e32 v113, v113
	v_mul_f32_e32 v121, 0xbfb8aa3b, v122
	v_min_f32_e32 v121, 0x42700000, v121
	v_exp_f32_e32 v121, v121
	v_mul_f32_e32 v113, v114, v113
	v_add_f32_e32 v114, 1.0, v120
	v_rcp_f32_e32 v114, v114
	v_mul_f32_e32 v122, 0xbfb8aa3b, v123
	v_min_f32_e32 v122, 0x42700000, v122
	v_exp_f32_e32 v122, v122
	v_mul_f32_e32 v114, v115, v114
	v_add_f32_e32 v115, 1.0, v121
	v_rcp_f32_e32 v115, v115
	v_mul_f32_e32 v123, 0xbfb8aa3b, v124
	v_min_f32_e32 v123, 0x42700000, v123
	v_exp_f32_e32 v123, v123
	v_mul_f32_e32 v115, v108, v115
	v_add_f32_e32 v108, 1.0, v122
	v_rcp_f32_e32 v108, v108
	v_mul_f32_e32 v124, 0xbfb8aa3b, v125
	v_min_f32_e32 v124, 0x42700000, v124
	v_exp_f32_e32 v124, v124
	v_mul_f32_e32 v116, v109, v108
	v_add_f32_e32 v108, 1.0, v123
	v_rcp_f32_e32 v108, v108
	v_mov_b32_e32 v109, 0
	v_cvt_pk_fp8_f32 v109, v115, v116
	v_mul_f32_e32 v110, v110, v108
	v_add_f32_e32 v108, 1.0, v124
	v_rcp_f32_e32 v108, v108
	s_nop 0
	v_mul_f32_e32 v111, v111, v108
	v_mov_b32_e32 v108, 0
	v_cvt_pk_fp8_f32 v108, v11, v112
	v_cvt_pk_fp8_f32 v109, v110, v111 op_sel:[0,0,1]
	v_cvt_pk_f32_fp8_sdwa v[110:111], v158 src0_sel:WORD_1
	v_cvt_pk_fp8_f32 v108, v113, v114 op_sel:[0,0,1]
	v_cvt_pk_f32_fp8_e32 v[112:113], v159
	v_cvt_pk_f32_fp8_sdwa v[114:115], v159 src0_sel:WORD_1
	global_store_dwordx2 v[118:119], v[108:109], off offset:128
	v_cvt_pk_f32_fp8_e32 v[108:109], v158
	v_mul_f32_e32 v11, 0xbfb8aa3b, v108
	v_min_f32_e32 v11, 0x42700000, v11
	v_exp_f32_e32 v11, v11
	v_mul_f32_e32 v108, 0xbfb8aa3b, v109
	v_min_f32_e32 v108, 0x42700000, v108
	v_exp_f32_e32 v108, v108
	v_add_f32_e32 v11, 1.0, v11
	v_rcp_f32_e32 v11, v11
	v_mul_f32_e32 v109, 0xbfb8aa3b, v110
	v_min_f32_e32 v109, 0x42700000, v109
	v_exp_f32_e32 v109, v109
	v_mul_f32_e32 v11, v104, v11
	v_add_f32_e32 v104, 1.0, v108
	v_rcp_f32_e32 v104, v104
	v_mul_f32_e32 v110, 0xbfb8aa3b, v111
	v_min_f32_e32 v110, 0x42700000, v110
	v_exp_f32_e32 v110, v110
	v_mul_f32_e32 v104, v105, v104
	v_add_f32_e32 v105, 1.0, v109
	v_rcp_f32_e32 v105, v105
	v_mul_f32_e32 v111, 0xbfb8aa3b, v112
	v_min_f32_e32 v111, 0x42700000, v111
	v_exp_f32_e32 v111, v111
	v_mul_f32_e32 v105, v106, v105
	v_add_f32_e32 v106, 1.0, v110
	v_rcp_f32_e32 v106, v106
	v_mul_f32_e32 v112, 0xbfb8aa3b, v113
	v_min_f32_e32 v112, 0x42700000, v112
	v_exp_f32_e32 v112, v112
	v_mul_f32_e32 v106, v107, v106
	v_add_f32_e32 v107, 1.0, v111
	v_rcp_f32_e32 v107, v107
	v_mul_f32_e32 v113, 0xbfb8aa3b, v114
	v_min_f32_e32 v113, 0x42700000, v113
	v_exp_f32_e32 v113, v113
	v_mul_f32_e32 v107, v100, v107
	v_add_f32_e32 v100, 1.0, v112
	v_rcp_f32_e32 v100, v100
	v_mul_f32_e32 v114, 0xbfb8aa3b, v115
	v_min_f32_e32 v114, 0x42700000, v114
	v_exp_f32_e32 v114, v114
	v_mul_f32_e32 v108, v101, v100
	v_add_f32_e32 v100, 1.0, v113
	v_rcp_f32_e32 v100, v100
	v_mov_b32_e32 v101, 0
	v_cvt_pk_fp8_f32 v101, v107, v108
	v_cvt_pk_f32_fp8_sdwa v[108:109], v157 src0_sel:WORD_1
	v_mul_f32_e32 v102, v102, v100
	v_add_f32_e32 v100, 1.0, v114
	v_rcp_f32_e32 v100, v100
	s_nop 0
	v_mul_f32_e32 v103, v103, v100
	v_mov_b32_e32 v100, 0
	v_cvt_pk_fp8_f32 v100, v11, v104
	v_cvt_pk_fp8_f32 v101, v102, v103 op_sel:[0,0,1]
	v_add_co_u32_e32 v104, vcc, s74, v2
	v_cvt_pk_fp8_f32 v100, v105, v106 op_sel:[0,0,1]
	s_nop 0
	v_addc_co_u32_e32 v105, vcc, 0, v3, vcc
	v_cvt_pk_f32_fp8_e32 v[106:107], v157
	global_store_dwordx2 v[104:105], v[100:101], off
	v_cvt_pk_f32_fp8_e32 v[100:101], v156
	v_cvt_pk_f32_fp8_sdwa v[104:105], v156 src0_sel:WORD_1
	v_lshl_add_u64 v[102:103], v[2:3], 0, s[0:1]
	s_mov_b64 s[0:1], 0xc000
	v_mul_f32_e32 v11, 0xbfb8aa3b, v100
	v_min_f32_e32 v11, 0x42700000, v11
	v_exp_f32_e32 v11, v11
	v_mul_f32_e32 v100, 0xbfb8aa3b, v101
	v_min_f32_e32 v100, 0x42700000, v100
	v_exp_f32_e32 v100, v100
	v_add_f32_e32 v11, 1.0, v11
	v_rcp_f32_e32 v11, v11
	v_mul_f32_e32 v101, 0xbfb8aa3b, v104
	v_min_f32_e32 v101, 0x42700000, v101
	v_exp_f32_e32 v101, v101
	v_mul_f32_e32 v11, v96, v11
	v_add_f32_e32 v96, 1.0, v100
	v_rcp_f32_e32 v96, v96
	v_mul_f32_e32 v104, 0xbfb8aa3b, v105
	v_min_f32_e32 v104, 0x42700000, v104
	v_exp_f32_e32 v104, v104
	v_mul_f32_e32 v96, v97, v96
	v_add_f32_e32 v97, 1.0, v101
	v_rcp_f32_e32 v97, v97
	v_mul_f32_e32 v105, 0xbfb8aa3b, v106
	v_min_f32_e32 v105, 0x42700000, v105
	v_exp_f32_e32 v105, v105
	v_mul_f32_e32 v97, v98, v97
	v_add_f32_e32 v98, 1.0, v104
	v_rcp_f32_e32 v98, v98
	v_mul_f32_e32 v106, 0xbfb8aa3b, v107
	v_min_f32_e32 v106, 0x42700000, v106
	v_exp_f32_e32 v106, v106
	v_mul_f32_e32 v98, v99, v98
	v_add_f32_e32 v99, 1.0, v105
	v_rcp_f32_e32 v99, v99
	v_mul_f32_e32 v107, 0xbfb8aa3b, v108
	v_min_f32_e32 v107, 0x42700000, v107
	v_exp_f32_e32 v107, v107
	v_mul_f32_e32 v99, v92, v99
	v_add_f32_e32 v92, 1.0, v106
	v_rcp_f32_e32 v92, v92
	v_mul_f32_e32 v108, 0xbfb8aa3b, v109
	v_min_f32_e32 v108, 0x42700000, v108
	v_exp_f32_e32 v108, v108
	v_mul_f32_e32 v100, v93, v92
	v_add_f32_e32 v92, 1.0, v107
	v_rcp_f32_e32 v92, v92
	v_mov_b32_e32 v93, 0
	v_cvt_pk_fp8_f32 v93, v99, v100
	v_mul_f32_e32 v94, v94, v92
	v_add_f32_e32 v92, 1.0, v108
	v_rcp_f32_e32 v92, v92
	s_nop 0
	v_mul_f32_e32 v95, v95, v92
	v_mov_b32_e32 v92, 0
	v_cvt_pk_fp8_f32 v92, v11, v96
	v_cvt_pk_fp8_f32 v93, v94, v95 op_sel:[0,0,1]
	s_nop 0
	v_cvt_pk_f32_fp8_sdwa v[94:95], v8 src0_sel:WORD_1
	v_cvt_pk_fp8_f32 v92, v97, v98 op_sel:[0,0,1]
	v_cvt_pk_f32_fp8_e32 v[96:97], v9
	global_store_dwordx2 v[102:103], v[92:93], off offset:128
	v_cvt_pk_f32_fp8_e32 v[92:93], v8
	v_cvt_pk_f32_fp8_sdwa v[8:9], v9 src0_sel:WORD_1
	v_mul_f32_e32 v11, 0xbfb8aa3b, v92
	v_min_f32_e32 v11, 0x42700000, v11
	v_exp_f32_e32 v11, v11
	v_mul_f32_e32 v92, 0xbfb8aa3b, v93
	v_min_f32_e32 v92, 0x42700000, v92
	v_exp_f32_e32 v92, v92
	v_add_f32_e32 v11, 1.0, v11
	v_rcp_f32_e32 v11, v11
	v_mul_f32_e32 v93, 0xbfb8aa3b, v94
	v_min_f32_e32 v93, 0x42700000, v93
	v_exp_f32_e32 v93, v93
	v_mul_f32_e32 v11, v88, v11
	v_add_f32_e32 v88, 1.0, v92
	v_rcp_f32_e32 v88, v88
	v_mul_f32_e32 v94, 0xbfb8aa3b, v95
	v_min_f32_e32 v94, 0x42700000, v94
	v_exp_f32_e32 v94, v94
	v_mul_f32_e32 v88, v89, v88
	v_add_f32_e32 v89, 1.0, v93
	v_rcp_f32_e32 v89, v89
	v_mul_f32_e32 v95, 0xbfb8aa3b, v96
	v_mul_f32_e32 v8, 0xbfb8aa3b, v8
	v_min_f32_e32 v95, 0x42700000, v95
	v_min_f32_e32 v8, 0x42700000, v8
	v_mul_f32_e32 v89, v90, v89
	v_add_f32_e32 v90, 1.0, v94
	v_exp_f32_e32 v95, v95
	v_exp_f32_e32 v8, v8
	v_rcp_f32_e32 v90, v90
	v_mul_f32_e32 v96, 0xbfb8aa3b, v97
	v_mul_f32_e32 v9, 0xbfb8aa3b, v9
	v_min_f32_e32 v96, 0x42700000, v96
	v_min_f32_e32 v9, 0x42700000, v9
	v_mul_f32_e32 v90, v91, v90
	v_add_f32_e32 v91, 1.0, v95
	v_add_f32_e32 v8, 1.0, v8
	v_exp_f32_e32 v96, v96
	v_exp_f32_e32 v9, v9
	v_rcp_f32_e32 v91, v91
	v_rcp_f32_e32 v8, v8
	v_mul_f32_e32 v84, v84, v91
	v_add_f32_e32 v91, 1.0, v96
	v_mul_f32_e32 v86, v86, v8
	v_add_f32_e32 v8, 1.0, v9
	v_rcp_f32_e32 v91, v91
	v_rcp_f32_e32 v8, v8
	v_mov_b32_e32 v9, 0
	v_mul_f32_e32 v85, v85, v91
	v_mul_f32_e32 v87, v87, v8
	v_mov_b32_e32 v8, 0
	v_cvt_pk_fp8_f32 v8, v11, v88
	v_cvt_pk_fp8_f32 v9, v84, v85
	v_lshl_add_u64 v[84:85], v[2:3], 0, s[0:1]
	s_mov_b32 s0, 0xc000
	v_cvt_pk_fp8_f32 v8, v89, v90 op_sel:[0,0,1]
	v_cvt_pk_fp8_f32 v9, v86, v87 op_sel:[0,0,1]
	v_add_co_u32_e32 v86, vcc, s0, v2
	v_cvt_pk_f32_fp8_e32 v[88:89], v7
	s_nop 0
	v_addc_co_u32_e32 v87, vcc, 0, v3, vcc
	global_store_dwordx2 v[86:87], v[8:9], off
	v_cvt_pk_f32_fp8_e32 v[8:9], v6
	v_cvt_pk_f32_fp8_sdwa v[86:87], v6 src0_sel:WORD_1
	v_cvt_pk_f32_fp8_sdwa v[6:7], v7 src0_sel:WORD_1
	s_mov_b64 s[0:1], 0x20000
	v_mul_f32_e32 v9, 0xbfb8aa3b, v9
	v_min_f32_e32 v9, 0x42700000, v9
	v_exp_f32_e32 v9, v9
	v_mul_f32_e32 v11, 0xbfb8aa3b, v86
	v_mul_f32_e32 v86, 0xbfb8aa3b, v87
	v_mul_f32_e32 v87, 0xbfb8aa3b, v88
	v_mul_f32_e32 v6, 0xbfb8aa3b, v6
	v_min_f32_e32 v87, 0x42700000, v87
	v_min_f32_e32 v6, 0x42700000, v6
	v_add_f32_e32 v9, 1.0, v9
	v_exp_f32_e32 v87, v87
	v_exp_f32_e32 v6, v6
	v_rcp_f32_e32 v9, v9
	v_mul_f32_e32 v8, 0xbfb8aa3b, v8
	v_min_f32_e32 v8, 0x42700000, v8
	v_mul_f32_e32 v88, 0xbfb8aa3b, v89
	v_mul_f32_e32 v7, 0xbfb8aa3b, v7
	v_exp_f32_e32 v8, v8
	v_min_f32_e32 v88, 0x42700000, v88
	v_min_f32_e32 v7, 0x42700000, v7
	v_mul_f32_e32 v9, v81, v9
	v_add_f32_e32 v81, 1.0, v87
	v_add_f32_e32 v6, 1.0, v6
	v_exp_f32_e32 v88, v88
	v_exp_f32_e32 v7, v7
	v_rcp_f32_e32 v81, v81
	v_rcp_f32_e32 v6, v6
	v_min_f32_e32 v11, 0x42700000, v11
	v_min_f32_e32 v86, 0x42700000, v86
	v_add_f32_e32 v8, 1.0, v8
	v_exp_f32_e32 v11, v11
	v_exp_f32_e32 v86, v86
	v_rcp_f32_e32 v8, v8
	v_mul_f32_e32 v76, v76, v81
	v_add_f32_e32 v81, 1.0, v88
	v_mul_f32_e32 v78, v78, v6
	v_add_f32_e32 v6, 1.0, v7
	v_rcp_f32_e32 v81, v81
	v_rcp_f32_e32 v6, v6
	v_mul_f32_e32 v8, v80, v8
	v_add_f32_e32 v11, 1.0, v11
	v_add_f32_e32 v80, 1.0, v86
	v_rcp_f32_e32 v11, v11
	v_rcp_f32_e32 v80, v80
	v_mul_f32_e32 v77, v77, v81
	v_mul_f32_e32 v79, v79, v6
	v_mov_b32_e32 v6, 0
	v_mov_b32_e32 v7, 0
	v_cvt_pk_fp8_f32 v6, v8, v9
	v_cvt_pk_fp8_f32 v7, v76, v77
	v_mul_f32_e32 v11, v82, v11
	v_mul_f32_e32 v80, v83, v80
	v_cvt_pk_fp8_f32 v6, v11, v80 op_sel:[0,0,1]
	v_cvt_pk_fp8_f32 v7, v78, v79 op_sel:[0,0,1]
	global_store_dwordx2 v[84:85], v[6:7], off offset:128
	v_add_co_u32_e32 v6, vcc, s76, v4
	s_nop 1
	v_addc_co_u32_e32 v7, vcc, 0, v5, vcc
	v_mov_b64_e32 v[82:83], v[192:193]
	v_mov_b64_e32 v[84:85], v[194:195]
	v_add_co_u32_e32 v6, vcc, s77, v4
	s_nop 0
	v_cvt_pk_f32_fp8_e32 v[86:87], v82
	v_cvt_pk_f32_fp8_sdwa v[88:89], v82 src0_sel:WORD_1
	v_cvt_pk_f32_fp8_e32 v[90:91], v83
	v_cvt_pk_f32_fp8_sdwa v[82:83], v83 src0_sel:WORD_1
	v_mul_f32_e32 v11, 0xbfb8aa3b, v86
	v_min_f32_e32 v11, 0x42700000, v11
	v_exp_f32_e32 v11, v11
	v_mul_f32_e32 v86, 0xbfb8aa3b, v87
	v_min_f32_e32 v86, 0x42700000, v86
	v_exp_f32_e32 v86, v86
	v_add_f32_e32 v11, 1.0, v11
	v_rcp_f32_e32 v11, v11
	v_mul_f32_e32 v87, 0xbfb8aa3b, v88
	v_min_f32_e32 v87, 0x42700000, v87
	v_exp_f32_e32 v87, v87
	v_mul_f32_e32 v11, v72, v11
	v_add_f32_e32 v72, 1.0, v86
	v_rcp_f32_e32 v72, v72
	v_mul_f32_e32 v88, 0xbfb8aa3b, v89
	v_min_f32_e32 v88, 0x42700000, v88
	v_exp_f32_e32 v88, v88
	v_mul_f32_e32 v72, v73, v72
	v_add_f32_e32 v73, 1.0, v87
	v_rcp_f32_e32 v73, v73
	v_mul_f32_e32 v89, 0xbfb8aa3b, v90
	v_min_f32_e32 v89, 0x42700000, v89
	v_exp_f32_e32 v89, v89
	v_mul_f32_e32 v73, v74, v73
	v_add_f32_e32 v74, 1.0, v88
	v_rcp_f32_e32 v74, v74
	v_mul_f32_e32 v90, 0xbfb8aa3b, v91
	v_min_f32_e32 v90, 0x42700000, v90
	v_exp_f32_e32 v90, v90
	v_mul_f32_e32 v74, v75, v74
	v_add_f32_e32 v75, 1.0, v89
	v_rcp_f32_e32 v75, v75
	v_mul_f32_e32 v82, 0xbfb8aa3b, v82
	v_min_f32_e32 v82, 0x42700000, v82
	v_exp_f32_e32 v82, v82
	v_mul_f32_e32 v75, v68, v75
	v_add_f32_e32 v68, 1.0, v90
	v_rcp_f32_e32 v68, v68
	v_addc_co_u32_e32 v7, vcc, 0, v5, vcc
	v_mov_b64_e32 v[80:81], v[196:197]
	v_mov_b64_e32 v[78:79], v[198:199]
	v_mul_f32_e32 v83, 0xbfb8aa3b, v83
	v_min_f32_e32 v83, 0x42700000, v83
	v_mul_f32_e32 v86, v69, v68
	v_add_f32_e32 v68, 1.0, v82
	v_exp_f32_e32 v83, v83
	v_rcp_f32_e32 v68, v68
	v_mov_b32_e32 v69, 0
	v_cvt_pk_fp8_f32 v69, v75, v86
	v_add_co_u32_e32 v6, vcc, s78, v4
	v_mul_f32_e32 v70, v70, v68
	v_add_f32_e32 v68, 1.0, v83
	v_rcp_f32_e32 v68, v68
	v_addc_co_u32_e32 v7, vcc, 0, v5, vcc
	v_add_co_u32_e32 v4, vcc, s79, v4
	v_mul_f32_e32 v71, v71, v68
	v_mov_b32_e32 v68, 0
	v_cvt_pk_fp8_f32 v68, v11, v72
	v_cvt_pk_fp8_f32 v69, v70, v71 op_sel:[0,0,1]
	v_addc_co_u32_e32 v5, vcc, 0, v5, vcc
	v_cvt_pk_fp8_f32 v68, v73, v74 op_sel:[0,0,1]
	v_lshl_add_u64 v[70:71], v[2:3], 0, s[0:1]
	s_mov_b32 s0, 0x20000
	v_add_co_u32_e32 v72, vcc, s0, v2
	v_mov_b64_e32 v[76:77], v[200:201]
	v_mov_b64_e32 v[8:9], v[202:203]
	v_addc_co_u32_e32 v73, vcc, 0, v3, vcc
	v_mov_b64_e32 v[6:7], v[204:205]
	s_nop 0
	v_mov_b64_e32 v[4:5], v[206:207]
	v_cvt_pk_f32_fp8_e32 v[74:75], v85
	global_store_dwordx2 v[72:73], v[68:69], off
	v_cvt_pk_f32_fp8_e32 v[68:69], v84
	v_cvt_pk_f32_fp8_sdwa v[72:73], v84 src0_sel:WORD_1
	v_cvt_pk_f32_fp8_sdwa v[82:83], v85 src0_sel:WORD_1
	s_mov_b64 s[0:1], 0x24000
	v_mul_f32_e32 v11, 0xbfb8aa3b, v68
	v_min_f32_e32 v11, 0x42700000, v11
	v_exp_f32_e32 v11, v11
	v_mul_f32_e32 v68, 0xbfb8aa3b, v69
	v_min_f32_e32 v68, 0x42700000, v68
	v_exp_f32_e32 v68, v68
	v_add_f32_e32 v11, 1.0, v11
	v_rcp_f32_e32 v11, v11
	v_mul_f32_e32 v69, 0xbfb8aa3b, v72
	v_min_f32_e32 v69, 0x42700000, v69
	v_exp_f32_e32 v69, v69
	v_mul_f32_e32 v11, v64, v11
	v_add_f32_e32 v64, 1.0, v68
	v_rcp_f32_e32 v64, v64
	v_mul_f32_e32 v72, 0xbfb8aa3b, v73
	v_min_f32_e32 v72, 0x42700000, v72
	v_exp_f32_e32 v72, v72
	v_mul_f32_e32 v64, v65, v64
	v_add_f32_e32 v65, 1.0, v69
	v_rcp_f32_e32 v65, v65
	v_mul_f32_e32 v73, 0xbfb8aa3b, v74
	v_min_f32_e32 v73, 0x42700000, v73
	v_exp_f32_e32 v73, v73
	v_mul_f32_e32 v65, v66, v65
	v_add_f32_e32 v66, 1.0, v72
	v_rcp_f32_e32 v66, v66
	v_mul_f32_e32 v74, 0xbfb8aa3b, v75
	v_min_f32_e32 v74, 0x42700000, v74
	v_exp_f32_e32 v74, v74
	v_mul_f32_e32 v66, v67, v66
	v_add_f32_e32 v67, 1.0, v73
	v_rcp_f32_e32 v67, v67
	v_mul_f32_e32 v75, 0xbfb8aa3b, v82
	v_min_f32_e32 v75, 0x42700000, v75
	v_exp_f32_e32 v75, v75
	v_mul_f32_e32 v67, v60, v67
	v_add_f32_e32 v60, 1.0, v74
	v_rcp_f32_e32 v60, v60
	v_mul_f32_e32 v82, 0xbfb8aa3b, v83
	v_min_f32_e32 v82, 0x42700000, v82
	v_exp_f32_e32 v82, v82
	v_mul_f32_e32 v68, v61, v60
	v_add_f32_e32 v60, 1.0, v75
	v_rcp_f32_e32 v60, v60
	v_mov_b32_e32 v61, 0
	v_cvt_pk_fp8_f32 v61, v67, v68
	v_mul_f32_e32 v62, v62, v60
	v_add_f32_e32 v60, 1.0, v82
	v_rcp_f32_e32 v60, v60
	s_nop 0
	v_mul_f32_e32 v63, v63, v60
	v_mov_b32_e32 v60, 0
	v_cvt_pk_fp8_f32 v60, v11, v64
	v_cvt_pk_fp8_f32 v61, v62, v63 op_sel:[0,0,1]
	s_nop 0
	v_cvt_pk_f32_fp8_sdwa v[62:63], v80 src0_sel:WORD_1
	v_cvt_pk_fp8_f32 v60, v65, v66 op_sel:[0,0,1]
	v_cvt_pk_f32_fp8_e32 v[64:65], v81
	v_cvt_pk_f32_fp8_sdwa v[66:67], v81 src0_sel:WORD_1
	global_store_dwordx2 v[70:71], v[60:61], off offset:128
	v_cvt_pk_f32_fp8_e32 v[60:61], v80
	v_mul_f32_e32 v11, 0xbfb8aa3b, v60
	v_min_f32_e32 v11, 0x42700000, v11
	v_exp_f32_e32 v11, v11
	v_mul_f32_e32 v60, 0xbfb8aa3b, v61
	v_min_f32_e32 v60, 0x42700000, v60
	v_exp_f32_e32 v60, v60
	v_add_f32_e32 v11, 1.0, v11
	v_rcp_f32_e32 v11, v11
	v_mul_f32_e32 v61, 0xbfb8aa3b, v62
	v_min_f32_e32 v61, 0x42700000, v61
	v_exp_f32_e32 v61, v61
	v_mul_f32_e32 v11, v56, v11
	v_add_f32_e32 v56, 1.0, v60
	v_rcp_f32_e32 v56, v56
	v_mul_f32_e32 v62, 0xbfb8aa3b, v63
	v_min_f32_e32 v62, 0x42700000, v62
	v_exp_f32_e32 v62, v62
	v_mul_f32_e32 v56, v57, v56
	v_add_f32_e32 v57, 1.0, v61
	v_rcp_f32_e32 v57, v57
	v_mul_f32_e32 v63, 0xbfb8aa3b, v64
	v_min_f32_e32 v63, 0x42700000, v63
	v_exp_f32_e32 v63, v63
	v_mul_f32_e32 v57, v58, v57
	v_add_f32_e32 v58, 1.0, v62
	v_rcp_f32_e32 v58, v58
	v_mul_f32_e32 v64, 0xbfb8aa3b, v65
	v_min_f32_e32 v64, 0x42700000, v64
	v_exp_f32_e32 v64, v64
	v_mul_f32_e32 v58, v59, v58
	v_add_f32_e32 v59, 1.0, v63
	v_rcp_f32_e32 v59, v59
	v_mul_f32_e32 v65, 0xbfb8aa3b, v66
	v_min_f32_e32 v65, 0x42700000, v65
	v_exp_f32_e32 v65, v65
	v_mul_f32_e32 v59, v52, v59
	v_add_f32_e32 v52, 1.0, v64
	v_rcp_f32_e32 v52, v52
	v_mul_f32_e32 v66, 0xbfb8aa3b, v67
	v_min_f32_e32 v66, 0x42700000, v66
	v_exp_f32_e32 v66, v66
	v_mul_f32_e32 v60, v53, v52
	v_add_f32_e32 v52, 1.0, v65
	v_rcp_f32_e32 v52, v52
	v_mov_b32_e32 v53, 0
	v_cvt_pk_fp8_f32 v53, v59, v60
	v_cvt_pk_f32_fp8_sdwa v[60:61], v79 src0_sel:WORD_1
	v_mul_f32_e32 v54, v54, v52
	v_add_f32_e32 v52, 1.0, v66
	v_rcp_f32_e32 v52, v52
	s_nop 0
	v_mul_f32_e32 v55, v55, v52
	v_mov_b32_e32 v52, 0
	v_cvt_pk_fp8_f32 v52, v11, v56
	v_cvt_pk_fp8_f32 v53, v54, v55 op_sel:[0,0,1]
	v_lshl_add_u64 v[54:55], v[2:3], 0, s[0:1]
	s_mov_b32 s0, 0x24000
	v_cvt_pk_fp8_f32 v52, v57, v58 op_sel:[0,0,1]
	v_add_co_u32_e32 v56, vcc, s0, v2
	v_cvt_pk_f32_fp8_e32 v[58:59], v79
	s_nop 0
	v_addc_co_u32_e32 v57, vcc, 0, v3, vcc
	global_store_dwordx2 v[56:57], v[52:53], off
	v_cvt_pk_f32_fp8_e32 v[52:53], v78
	v_cvt_pk_f32_fp8_sdwa v[56:57], v78 src0_sel:WORD_1
	s_mov_b64 s[0:1], 0x28000
	v_mul_f32_e32 v11, 0xbfb8aa3b, v52
	v_min_f32_e32 v11, 0x42700000, v11
	v_exp_f32_e32 v11, v11
	v_mul_f32_e32 v52, 0xbfb8aa3b, v53
	v_min_f32_e32 v52, 0x42700000, v52
	v_exp_f32_e32 v52, v52
	v_add_f32_e32 v11, 1.0, v11
	v_rcp_f32_e32 v11, v11
	v_mul_f32_e32 v53, 0xbfb8aa3b, v56
	v_min_f32_e32 v53, 0x42700000, v53
	v_exp_f32_e32 v53, v53
	v_mul_f32_e32 v11, v48, v11
	v_add_f32_e32 v48, 1.0, v52
	v_rcp_f32_e32 v48, v48
	v_mul_f32_e32 v56, 0xbfb8aa3b, v57
	v_min_f32_e32 v56, 0x42700000, v56
	v_exp_f32_e32 v56, v56
	v_mul_f32_e32 v48, v49, v48
	v_add_f32_e32 v49, 1.0, v53
	v_rcp_f32_e32 v49, v49
	v_mul_f32_e32 v57, 0xbfb8aa3b, v58
	v_min_f32_e32 v57, 0x42700000, v57
	v_exp_f32_e32 v57, v57
	v_mul_f32_e32 v49, v50, v49
	v_add_f32_e32 v50, 1.0, v56
	v_rcp_f32_e32 v50, v50
	v_mul_f32_e32 v58, 0xbfb8aa3b, v59
	v_min_f32_e32 v58, 0x42700000, v58
	v_exp_f32_e32 v58, v58
	v_mul_f32_e32 v50, v51, v50
	v_add_f32_e32 v51, 1.0, v57
	v_rcp_f32_e32 v51, v51
	v_mul_f32_e32 v59, 0xbfb8aa3b, v60
	v_min_f32_e32 v59, 0x42700000, v59
	v_exp_f32_e32 v59, v59
	v_mul_f32_e32 v51, v44, v51
	v_add_f32_e32 v44, 1.0, v58
	v_rcp_f32_e32 v44, v44
	v_mul_f32_e32 v60, 0xbfb8aa3b, v61
	v_min_f32_e32 v60, 0x42700000, v60
	v_exp_f32_e32 v60, v60
	v_mul_f32_e32 v52, v45, v44
	v_add_f32_e32 v44, 1.0, v59
	v_rcp_f32_e32 v44, v44
	v_mov_b32_e32 v45, 0
	v_cvt_pk_fp8_f32 v45, v51, v52
	v_mul_f32_e32 v46, v46, v44
	v_add_f32_e32 v44, 1.0, v60
	v_rcp_f32_e32 v44, v44
	s_nop 0
	v_mul_f32_e32 v47, v47, v44
	v_mov_b32_e32 v44, 0
	v_cvt_pk_fp8_f32 v44, v11, v48
	v_cvt_pk_fp8_f32 v45, v46, v47 op_sel:[0,0,1]
	v_cvt_pk_f32_fp8_sdwa v[46:47], v76 src0_sel:WORD_1
	v_cvt_pk_fp8_f32 v44, v49, v50 op_sel:[0,0,1]
	v_cvt_pk_f32_fp8_e32 v[48:49], v77
	v_cvt_pk_f32_fp8_sdwa v[50:51], v77 src0_sel:WORD_1
	global_store_dwordx2 v[54:55], v[44:45], off offset:128
	v_cvt_pk_f32_fp8_e32 v[44:45], v76
	v_mul_f32_e32 v11, 0xbfb8aa3b, v44
	v_min_f32_e32 v11, 0x42700000, v11
	v_exp_f32_e32 v11, v11
	v_mul_f32_e32 v44, 0xbfb8aa3b, v45
	v_min_f32_e32 v44, 0x42700000, v44
	v_exp_f32_e32 v44, v44
	v_add_f32_e32 v11, 1.0, v11
	v_rcp_f32_e32 v11, v11
	v_mul_f32_e32 v45, 0xbfb8aa3b, v46
	v_min_f32_e32 v45, 0x42700000, v45
	v_exp_f32_e32 v45, v45
	v_mul_f32_e32 v11, v40, v11
	v_add_f32_e32 v40, 1.0, v44
	v_rcp_f32_e32 v40, v40
	v_mul_f32_e32 v46, 0xbfb8aa3b, v47
	v_min_f32_e32 v46, 0x42700000, v46
	v_exp_f32_e32 v46, v46
	v_mul_f32_e32 v40, v41, v40
	v_add_f32_e32 v41, 1.0, v45
	v_rcp_f32_e32 v41, v41
	v_mul_f32_e32 v47, 0xbfb8aa3b, v48
	v_min_f32_e32 v47, 0x42700000, v47
	v_exp_f32_e32 v47, v47
	v_mul_f32_e32 v41, v42, v41
	v_add_f32_e32 v42, 1.0, v46
	v_rcp_f32_e32 v42, v42
	v_mul_f32_e32 v48, 0xbfb8aa3b, v49
	v_min_f32_e32 v48, 0x42700000, v48
	v_exp_f32_e32 v48, v48
	v_mul_f32_e32 v42, v43, v42
	v_add_f32_e32 v43, 1.0, v47
	v_rcp_f32_e32 v43, v43
	v_mul_f32_e32 v49, 0xbfb8aa3b, v50
	v_min_f32_e32 v49, 0x42700000, v49
	v_exp_f32_e32 v49, v49
	v_mul_f32_e32 v43, v36, v43
	v_add_f32_e32 v36, 1.0, v48
	v_rcp_f32_e32 v36, v36
	v_mul_f32_e32 v50, 0xbfb8aa3b, v51
	v_min_f32_e32 v50, 0x42700000, v50
	v_exp_f32_e32 v50, v50
	v_mul_f32_e32 v44, v37, v36
	v_add_f32_e32 v36, 1.0, v49
	v_rcp_f32_e32 v36, v36
	v_mov_b32_e32 v37, 0
	v_cvt_pk_fp8_f32 v37, v43, v44
	v_mul_f32_e32 v38, v38, v36
	v_add_f32_e32 v36, 1.0, v50
	v_rcp_f32_e32 v36, v36
	s_nop 0
	v_mul_f32_e32 v39, v39, v36
	v_mov_b32_e32 v36, 0
	v_cvt_pk_fp8_f32 v36, v11, v40
	v_cvt_pk_fp8_f32 v37, v38, v39 op_sel:[0,0,1]
	v_lshl_add_u64 v[38:39], v[2:3], 0, s[0:1]
	s_mov_b32 s0, 0x28000
	v_cvt_pk_fp8_f32 v36, v41, v42 op_sel:[0,0,1]
	v_add_co_u32_e32 v40, vcc, s0, v2
	v_cvt_pk_f32_fp8_e32 v[42:43], v9
	s_nop 0
	v_addc_co_u32_e32 v41, vcc, 0, v3, vcc
	global_store_dwordx2 v[40:41], v[36:37], off
	v_cvt_pk_f32_fp8_e32 v[36:37], v8
	v_cvt_pk_f32_fp8_sdwa v[40:41], v8 src0_sel:WORD_1
	v_cvt_pk_f32_fp8_sdwa v[8:9], v9 src0_sel:WORD_1
	s_mov_b64 s[0:1], 0x2c000
	v_mul_f32_e32 v11, 0xbfb8aa3b, v36
	v_min_f32_e32 v11, 0x42700000, v11
	v_exp_f32_e32 v11, v11
	v_mul_f32_e32 v36, 0xbfb8aa3b, v37
	v_min_f32_e32 v36, 0x42700000, v36
	v_exp_f32_e32 v36, v36
	v_add_f32_e32 v11, 1.0, v11
	v_rcp_f32_e32 v11, v11
	v_mul_f32_e32 v37, 0xbfb8aa3b, v40
	v_min_f32_e32 v37, 0x42700000, v37
	v_exp_f32_e32 v37, v37
	v_mul_f32_e32 v11, v32, v11
	v_add_f32_e32 v32, 1.0, v36
	v_rcp_f32_e32 v32, v32
	v_mul_f32_e32 v40, 0xbfb8aa3b, v41
	v_min_f32_e32 v40, 0x42700000, v40
	v_exp_f32_e32 v40, v40
	v_mul_f32_e32 v32, v33, v32
	v_add_f32_e32 v33, 1.0, v37
	v_rcp_f32_e32 v33, v33
	v_mul_f32_e32 v41, 0xbfb8aa3b, v42
	v_mul_f32_e32 v8, 0xbfb8aa3b, v8
	v_min_f32_e32 v41, 0x42700000, v41
	v_min_f32_e32 v8, 0x42700000, v8
	v_mul_f32_e32 v33, v34, v33
	v_add_f32_e32 v34, 1.0, v40
	v_exp_f32_e32 v41, v41
	v_exp_f32_e32 v8, v8
	v_rcp_f32_e32 v34, v34
	v_mul_f32_e32 v42, 0xbfb8aa3b, v43
	v_mul_f32_e32 v9, 0xbfb8aa3b, v9
	v_min_f32_e32 v42, 0x42700000, v42
	v_min_f32_e32 v9, 0x42700000, v9
	v_mul_f32_e32 v34, v35, v34
	v_add_f32_e32 v35, 1.0, v41
	v_add_f32_e32 v8, 1.0, v8
	v_exp_f32_e32 v42, v42
	v_exp_f32_e32 v9, v9
	v_rcp_f32_e32 v35, v35
	v_rcp_f32_e32 v8, v8
	v_mul_f32_e32 v28, v28, v35
	v_add_f32_e32 v35, 1.0, v42
	v_mul_f32_e32 v30, v30, v8
	v_add_f32_e32 v8, 1.0, v9
	v_rcp_f32_e32 v35, v35
	v_rcp_f32_e32 v8, v8
	v_mov_b32_e32 v9, 0
	v_mul_f32_e32 v29, v29, v35
	v_mul_f32_e32 v31, v31, v8
	v_mov_b32_e32 v8, 0
	v_cvt_pk_fp8_f32 v8, v11, v32
	v_cvt_pk_fp8_f32 v9, v28, v29
	v_cvt_pk_f32_fp8_sdwa v[28:29], v6 src0_sel:WORD_1
	v_cvt_pk_fp8_f32 v8, v33, v34 op_sel:[0,0,1]
	v_cvt_pk_fp8_f32 v9, v30, v31 op_sel:[0,0,1]
	v_cvt_pk_f32_fp8_e32 v[30:31], v7
	v_mul_f32_e32 v11, 0xbfb8aa3b, v28
	v_mul_f32_e32 v28, 0xbfb8aa3b, v29
	global_store_dwordx2 v[38:39], v[8:9], off offset:128
	v_cvt_pk_f32_fp8_e32 v[8:9], v6
	v_cvt_pk_f32_fp8_sdwa v[6:7], v7 src0_sel:WORD_1
	v_mul_f32_e32 v29, 0xbfb8aa3b, v30
	v_min_f32_e32 v29, 0x42700000, v29
	v_mul_f32_e32 v9, 0xbfb8aa3b, v9
	v_min_f32_e32 v9, 0x42700000, v9
	v_exp_f32_e32 v9, v9
	v_mul_f32_e32 v6, 0xbfb8aa3b, v6
	v_min_f32_e32 v6, 0x42700000, v6
	v_exp_f32_e32 v29, v29
	v_add_f32_e32 v9, 1.0, v9
	v_exp_f32_e32 v6, v6
	v_rcp_f32_e32 v9, v9
	v_mul_f32_e32 v8, 0xbfb8aa3b, v8
	v_min_f32_e32 v8, 0x42700000, v8
	v_mul_f32_e32 v30, 0xbfb8aa3b, v31
	v_mul_f32_e32 v7, 0xbfb8aa3b, v7
	v_exp_f32_e32 v8, v8
	v_min_f32_e32 v30, 0x42700000, v30
	v_min_f32_e32 v7, 0x42700000, v7
	v_mul_f32_e32 v9, v25, v9
	v_add_f32_e32 v25, 1.0, v29
	v_add_f32_e32 v6, 1.0, v6
	v_exp_f32_e32 v30, v30
	v_exp_f32_e32 v7, v7
	v_rcp_f32_e32 v25, v25
	v_rcp_f32_e32 v6, v6
	v_min_f32_e32 v11, 0x42700000, v11
	v_min_f32_e32 v28, 0x42700000, v28
	v_add_f32_e32 v8, 1.0, v8
	v_exp_f32_e32 v11, v11
	v_exp_f32_e32 v28, v28
	v_rcp_f32_e32 v8, v8
	v_mul_f32_e32 v20, v20, v25
	v_add_f32_e32 v25, 1.0, v30
	v_mul_f32_e32 v22, v22, v6
	v_add_f32_e32 v6, 1.0, v7
	v_rcp_f32_e32 v25, v25
	v_rcp_f32_e32 v6, v6
	v_mul_f32_e32 v8, v24, v8
	v_add_f32_e32 v11, 1.0, v11
	v_add_f32_e32 v24, 1.0, v28
	v_rcp_f32_e32 v11, v11
	v_rcp_f32_e32 v24, v24
	v_mul_f32_e32 v21, v21, v25
	v_mul_f32_e32 v23, v23, v6
	v_mov_b32_e32 v6, 0
	v_mov_b32_e32 v7, 0
	v_cvt_pk_fp8_f32 v6, v8, v9
	v_cvt_pk_fp8_f32 v7, v20, v21
	v_mul_f32_e32 v11, v26, v11
	v_mul_f32_e32 v24, v27, v24
	v_cvt_pk_fp8_f32 v6, v11, v24 op_sel:[0,0,1]
	v_cvt_pk_fp8_f32 v7, v22, v23 op_sel:[0,0,1]
	v_lshl_add_u64 v[8:9], v[2:3], 0, s[0:1]
	s_mov_b32 s0, 0x2c000
	v_add_co_u32_e32 v2, vcc, s0, v2
	v_cvt_pk_f32_fp8_e32 v[20:21], v5
	s_nop 0
	v_addc_co_u32_e32 v3, vcc, 0, v3, vcc
	global_store_dwordx2 v[2:3], v[6:7], off
	v_cvt_pk_f32_fp8_e32 v[2:3], v4
	v_cvt_pk_f32_fp8_sdwa v[6:7], v4 src0_sel:WORD_1
	v_mul_f32_e32 v11, 0xbfb8aa3b, v20
	v_min_f32_e32 v11, 0x42700000, v11
	v_mul_f32_e32 v2, 0xbfb8aa3b, v2
	v_min_f32_e32 v2, 0x42700000, v2
	v_exp_f32_e32 v2, v2
	v_mul_f32_e32 v3, 0xbfb8aa3b, v3
	v_min_f32_e32 v3, 0x42700000, v3
	v_exp_f32_e32 v3, v3
	v_add_f32_e32 v2, 1.0, v2
	v_rcp_f32_e32 v2, v2
	v_mul_f32_e32 v6, 0xbfb8aa3b, v6
	v_min_f32_e32 v6, 0x42700000, v6
	v_exp_f32_e32 v6, v6
	v_mul_f32_e32 v16, v16, v2
	v_add_f32_e32 v2, 1.0, v3
	v_rcp_f32_e32 v2, v2
	v_mul_f32_e32 v7, 0xbfb8aa3b, v7
	v_min_f32_e32 v7, 0x42700000, v7
	v_exp_f32_e32 v7, v7
	v_mul_f32_e32 v3, v17, v2
	v_add_f32_e32 v2, 1.0, v6
	v_rcp_f32_e32 v2, v2
	v_exp_f32_e32 v11, v11
	v_mul_f32_e32 v20, 0xbfb8aa3b, v21
	v_cvt_pk_f32_fp8_sdwa v[4:5], v5 src0_sel:WORD_1
	v_mul_f32_e32 v6, v18, v2
	v_add_f32_e32 v2, 1.0, v7
	v_rcp_f32_e32 v2, v2
	v_min_f32_e32 v20, 0x42700000, v20
	v_exp_f32_e32 v20, v20
	v_mul_f32_e32 v4, 0xbfb8aa3b, v4
	v_mul_f32_e32 v7, v19, v2
	v_add_f32_e32 v2, 1.0, v11
	v_rcp_f32_e32 v2, v2
	v_min_f32_e32 v4, 0x42700000, v4
	v_exp_f32_e32 v4, v4
	v_mul_f32_e32 v5, 0xbfb8aa3b, v5
	v_mul_f32_e32 v11, v12, v2
	v_add_f32_e32 v2, 1.0, v20
	v_rcp_f32_e32 v2, v2
	v_min_f32_e32 v5, 0x42700000, v5
	v_exp_f32_e32 v5, v5
	s_mov_b64 s[0:1], -1
	v_mul_f32_e32 v12, v13, v2
	v_add_f32_e32 v2, 1.0, v4
	v_rcp_f32_e32 v2, v2
	s_and_b64 vcc, exec, s[6:7]
	v_mul_f32_e32 v4, v14, v2
	v_add_f32_e32 v2, 1.0, v5
	v_rcp_f32_e32 v2, v2
	s_nop 0
	v_mul_f32_e32 v5, v15, v2
	v_mov_b32_e32 v2, 0
	v_cvt_pk_fp8_f32 v2, v16, v3
	v_mov_b32_e32 v3, 0
	v_cvt_pk_fp8_f32 v3, v11, v12
	v_cvt_pk_fp8_f32 v2, v6, v7 op_sel:[0,0,1]
	v_cvt_pk_fp8_f32 v3, v4, v5 op_sel:[0,0,1]
	global_store_dwordx2 v[8:9], v[2:3], off offset:128
	s_cbranch_vccnz .LBB0_877
	s_andn2_b64 vcc, exec, s[22:23]
	s_cbranch_vccnz .LBB0_876
	s_barrier
	s_branch .LBB0_876
